# baseline (speedup 1.0000x reference)
.LBB1_30:
	s_and_b64 vcc, exec, s[4:5]
	s_cbranch_vccz .LBB1_41
	s_load_dwordx4 s[44:47], s[0:1], 0x0
	s_load_dwordx2 s[48:49], s[0:1], 0x20
	s_add_i32 s50, s2, 0xffffff40
	v_and_b32_e32 v1, 31, v0
	v_lshrrev_b32_e32 v2, 5, v0
	v_lshlrev_b32_e32 v3, 5, v1
	v_lshl_add_u32 v3, v2, 13, v3
	v_add_u32_e32 v3, 0x1000, v3
	v_lshlrev_b32_e32 v4, 4, v1
	v_lshl_add_u32 v4, v2, 12, v4
	v_add_u32_e32 v4, 0x800, v4
	s_waitcnt lgkmcnt(0)
	s_add_u32 s48, s48, 0x408000
	s_addc_u32 s49, s49, 0
	s_load_dwordx4 s[52:55], s[48:49], 0x400
	s_lshl_b32 s51, s50, 18
	s_add_u32 s44, s44, s51
	s_addc_u32 s45, s45, 0
	s_mul_i32 s51, s50, 0x30000
	s_add_u32 s46, s46, s51
	s_addc_u32 s47, s47, 0
	s_waitcnt lgkmcnt(0)
	s_lshl_b32 s51, s50, 19
	s_add_u32 s52, s52, s51
	s_addc_u32 s53, s53, 0
	s_mul_i32 s51, s50, 0x60000
	s_add_u32 s54, s54, s51
	s_addc_u32 s55, s55, 0
	v_cmp_eq_u32_e64 s[78:79], 0, v0
	v_mov_b32_e32 v5, 1
	v_mov_b32_e32 v6, s50
	v_lshlrev_b32_e32 v6, 2, v6
	s_add_u32 s58, s52, 0x0
	s_addc_u32 s59, s53, 0
	global_load_dwordx4 v[16:19], v3, s[58:59] nt
	global_load_dwordx4 v[20:23], v3, s[58:59] offset:16 nt
	s_add_u32 s58, s52, 0x20000
	s_addc_u32 s59, s53, 0
	global_load_dwordx4 v[24:27], v3, s[58:59] nt
	global_load_dwordx4 v[28:31], v3, s[58:59] offset:16 nt
	s_add_u32 s58, s52, 0x40000
	s_addc_u32 s59, s53, 0
	global_load_dwordx4 v[32:35], v3, s[58:59] nt
	global_load_dwordx4 v[36:39], v3, s[58:59] offset:16 nt
	s_add_u32 s58, s52, 0x60000
	s_addc_u32 s59, s53, 0
	global_load_dwordx4 v[40:43], v3, s[58:59] nt
	global_load_dwordx4 v[44:47], v3, s[58:59] offset:16 nt
	s_add_u32 s58, s54, 0x0
	s_addc_u32 s59, s55, 0
	global_load_dwordx4 v[48:51], v3, s[58:59] nt
	global_load_dwordx4 v[52:55], v3, s[58:59] offset:16 nt
	s_add_u32 s58, s54, 0x20000
	s_addc_u32 s59, s55, 0
	global_load_dwordx4 v[56:59], v3, s[58:59] nt
	global_load_dwordx4 v[60:63], v3, s[58:59] offset:16 nt
	s_add_u32 s58, s54, 0x40000
	s_addc_u32 s59, s55, 0
	global_load_dwordx4 v[64:67], v3, s[58:59] nt
	global_load_dwordx4 v[68:71], v3, s[58:59] offset:16 nt
	s_add_u32 s58, s52, 0x400
	s_addc_u32 s59, s53, 0
	global_load_dwordx4 v[72:75], v3, s[58:59] nt
	global_load_dwordx4 v[76:79], v3, s[58:59] offset:16 nt
	s_add_u32 s58, s52, 0x20400
	s_addc_u32 s59, s53, 0
	global_load_dwordx4 v[80:83], v3, s[58:59] nt
	global_load_dwordx4 v[84:87], v3, s[58:59] offset:16 nt
	s_add_u32 s58, s52, 0x40400
	s_addc_u32 s59, s53, 0
	global_load_dwordx4 v[88:91], v3, s[58:59] nt
	global_load_dwordx4 v[92:95], v3, s[58:59] offset:16 nt
	s_add_u32 s58, s52, 0x60400
	s_addc_u32 s59, s53, 0
	global_load_dwordx4 v[96:99], v3, s[58:59] nt
	global_load_dwordx4 v[100:103], v3, s[58:59] offset:16 nt
	s_add_u32 s58, s54, 0x400
	s_addc_u32 s59, s55, 0
	global_load_dwordx4 v[104:107], v3, s[58:59] nt
	global_load_dwordx4 v[108:111], v3, s[58:59] offset:16 nt
	s_add_u32 s58, s54, 0x20400
	s_addc_u32 s59, s55, 0
	global_load_dwordx4 v[112:115], v3, s[58:59] nt
	global_load_dwordx4 v[116:119], v3, s[58:59] offset:16 nt
	s_add_u32 s58, s54, 0x40400
	s_addc_u32 s59, s55, 0
	global_load_dwordx4 v[120:123], v3, s[58:59] nt
	global_load_dwordx4 v[124:127], v3, s[58:59] offset:16 nt
	s_waitcnt vmcnt(26)
	v_cvt_pk_f16_f32 v16, v16, v17
	v_cvt_pk_f16_f32 v17, v18, v19
	v_cvt_pk_f16_f32 v18, v20, v21
	v_cvt_pk_f16_f32 v19, v22, v23
	s_add_u32 s76, s44, 0x0
	s_addc_u32 s77, s45, 0
	global_store_dwordx4 v4, v[16:19], s[76:77] sc1
	s_waitcnt vmcnt(25)
	v_cvt_pk_f16_f32 v24, v24, v25
	v_cvt_pk_f16_f32 v25, v26, v27
	v_cvt_pk_f16_f32 v26, v28, v29
	v_cvt_pk_f16_f32 v27, v30, v31
	s_add_u32 s76, s44, 0x10000
	s_addc_u32 s77, s45, 0
	global_store_dwordx4 v4, v[24:27], s[76:77] sc1
	s_waitcnt vmcnt(24)
	v_cvt_pk_f16_f32 v32, v32, v33
	v_cvt_pk_f16_f32 v33, v34, v35
	v_cvt_pk_f16_f32 v34, v36, v37
	v_cvt_pk_f16_f32 v35, v38, v39
	s_add_u32 s76, s44, 0x20000
	s_addc_u32 s77, s45, 0
	global_store_dwordx4 v4, v[32:35], s[76:77] sc1
	s_waitcnt vmcnt(23)
	v_cvt_pk_f16_f32 v40, v40, v41
	v_cvt_pk_f16_f32 v41, v42, v43
	v_cvt_pk_f16_f32 v42, v44, v45
	v_cvt_pk_f16_f32 v43, v46, v47
	s_add_u32 s76, s44, 0x30000
	s_addc_u32 s77, s45, 0
	global_store_dwordx4 v4, v[40:43], s[76:77] sc1
	s_waitcnt vmcnt(22)
	v_cvt_pk_f16_f32 v48, v48, v49
	v_cvt_pk_f16_f32 v49, v50, v51
	v_cvt_pk_f16_f32 v50, v52, v53
	v_cvt_pk_f16_f32 v51, v54, v55
	s_add_u32 s76, s46, 0x0
	s_addc_u32 s77, s47, 0
	global_store_dwordx4 v4, v[48:51], s[76:77] sc1
	s_waitcnt vmcnt(21)
	v_cvt_pk_f16_f32 v56, v56, v57
	v_cvt_pk_f16_f32 v57, v58, v59
	v_cvt_pk_f16_f32 v58, v60, v61
	v_cvt_pk_f16_f32 v59, v62, v63
	s_add_u32 s76, s46, 0x10000
	s_addc_u32 s77, s47, 0
	global_store_dwordx4 v4, v[56:59], s[76:77] sc1
	s_waitcnt vmcnt(20)
	v_cvt_pk_f16_f32 v64, v64, v65
	v_cvt_pk_f16_f32 v65, v66, v67
	v_cvt_pk_f16_f32 v66, v68, v69
	v_cvt_pk_f16_f32 v67, v70, v71
	s_add_u32 s76, s46, 0x20000
	s_addc_u32 s77, s47, 0
	global_store_dwordx4 v4, v[64:67], s[76:77] sc1
	s_add_u32 s58, s52, 0x800
	s_addc_u32 s59, s53, 0
	global_load_dwordx4 v[16:19], v3, s[58:59] nt
	global_load_dwordx4 v[20:23], v3, s[58:59] offset:16 nt
	s_add_u32 s58, s52, 0x20800
	s_addc_u32 s59, s53, 0
	global_load_dwordx4 v[24:27], v3, s[58:59] nt
	global_load_dwordx4 v[28:31], v3, s[58:59] offset:16 nt
	s_add_u32 s58, s52, 0x40800
	s_addc_u32 s59, s53, 0
	global_load_dwordx4 v[32:35], v3, s[58:59] nt
	global_load_dwordx4 v[36:39], v3, s[58:59] offset:16 nt
	s_add_u32 s58, s52, 0x60800
	s_addc_u32 s59, s53, 0
	global_load_dwordx4 v[40:43], v3, s[58:59] nt
	global_load_dwordx4 v[44:47], v3, s[58:59] offset:16 nt
	s_add_u32 s58, s54, 0x800
	s_addc_u32 s59, s55, 0
	global_load_dwordx4 v[48:51], v3, s[58:59] nt
	global_load_dwordx4 v[52:55], v3, s[58:59] offset:16 nt
	s_add_u32 s58, s54, 0x20800
	s_addc_u32 s59, s55, 0
	global_load_dwordx4 v[56:59], v3, s[58:59] nt
	global_load_dwordx4 v[60:63], v3, s[58:59] offset:16 nt
	s_add_u32 s58, s54, 0x40800
	s_addc_u32 s59, s55, 0
	global_load_dwordx4 v[64:67], v3, s[58:59] nt
	global_load_dwordx4 v[68:71], v3, s[58:59] offset:16 nt
	s_waitcnt vmcnt(33)
	v_cvt_pk_f16_f32 v72, v72, v73
	v_cvt_pk_f16_f32 v73, v74, v75
	v_cvt_pk_f16_f32 v74, v76, v77
	v_cvt_pk_f16_f32 v75, v78, v79
	s_add_u32 s76, s44, 0x200
	s_addc_u32 s77, s45, 0
	global_store_dwordx4 v4, v[72:75], s[76:77] sc1
	s_waitcnt vmcnt(32)
	v_cvt_pk_f16_f32 v80, v80, v81
	v_cvt_pk_f16_f32 v81, v82, v83
	v_cvt_pk_f16_f32 v82, v84, v85
	v_cvt_pk_f16_f32 v83, v86, v87
	s_add_u32 s76, s44, 0x10200
	s_addc_u32 s77, s45, 0
	global_store_dwordx4 v4, v[80:83], s[76:77] sc1
	s_waitcnt vmcnt(31)
	v_cvt_pk_f16_f32 v88, v88, v89
	v_cvt_pk_f16_f32 v89, v90, v91
	v_cvt_pk_f16_f32 v90, v92, v93
	v_cvt_pk_f16_f32 v91, v94, v95
	s_add_u32 s76, s44, 0x20200
	s_addc_u32 s77, s45, 0
	global_store_dwordx4 v4, v[88:91], s[76:77] sc1
	s_waitcnt vmcnt(30)
	v_cvt_pk_f16_f32 v96, v96, v97
	v_cvt_pk_f16_f32 v97, v98, v99
	v_cvt_pk_f16_f32 v98, v100, v101
	v_cvt_pk_f16_f32 v99, v102, v103
	s_add_u32 s76, s44, 0x30200
	s_addc_u32 s77, s45, 0
	global_store_dwordx4 v4, v[96:99], s[76:77] sc1
	s_waitcnt vmcnt(29)
	v_cvt_pk_f16_f32 v104, v104, v105
	v_cvt_pk_f16_f32 v105, v106, v107
	v_cvt_pk_f16_f32 v106, v108, v109
	v_cvt_pk_f16_f32 v107, v110, v111
	s_add_u32 s76, s46, 0x200
	s_addc_u32 s77, s47, 0
	global_store_dwordx4 v4, v[104:107], s[76:77] sc1
	s_waitcnt vmcnt(28)
	v_cvt_pk_f16_f32 v112, v112, v113
	v_cvt_pk_f16_f32 v113, v114, v115
	v_cvt_pk_f16_f32 v114, v116, v117
	v_cvt_pk_f16_f32 v115, v118, v119
	s_add_u32 s76, s46, 0x10200
	s_addc_u32 s77, s47, 0
	global_store_dwordx4 v4, v[112:115], s[76:77] sc1
	s_waitcnt vmcnt(27)
	v_cvt_pk_f16_f32 v120, v120, v121
	v_cvt_pk_f16_f32 v121, v122, v123
	v_cvt_pk_f16_f32 v122, v124, v125
	v_cvt_pk_f16_f32 v123, v126, v127
	s_add_u32 s76, s46, 0x20200
	s_addc_u32 s77, s47, 0
	global_store_dwordx4 v4, v[120:123], s[76:77] sc1
	s_waitcnt vmcnt(21)
	s_barrier
	s_mov_b64 s[56:57], exec
	s_and_b64 exec, exec, s[78:79]
	global_store_dword v6, v5, s[48:49] offset:0 sc1
	s_mov_b64 exec, s[56:57]
	s_add_u32 s58, s52, 0xc00
	s_addc_u32 s59, s53, 0
	global_load_dwordx4 v[72:75], v3, s[58:59] nt
	global_load_dwordx4 v[76:79], v3, s[58:59] offset:16 nt
	s_add_u32 s58, s52, 0x20c00
	s_addc_u32 s59, s53, 0
	global_load_dwordx4 v[80:83], v3, s[58:59] nt
	global_load_dwordx4 v[84:87], v3, s[58:59] offset:16 nt
	s_add_u32 s58, s52, 0x40c00
	s_addc_u32 s59, s53, 0
	global_load_dwordx4 v[88:91], v3, s[58:59] nt
	global_load_dwordx4 v[92:95], v3, s[58:59] offset:16 nt
	s_add_u32 s58, s52, 0x60c00
	s_addc_u32 s59, s53, 0
	global_load_dwordx4 v[96:99], v3, s[58:59] nt
	global_load_dwordx4 v[100:103], v3, s[58:59] offset:16 nt
	s_add_u32 s58, s54, 0xc00
	s_addc_u32 s59, s55, 0
	global_load_dwordx4 v[104:107], v3, s[58:59] nt
	global_load_dwordx4 v[108:111], v3, s[58:59] offset:16 nt
	s_add_u32 s58, s54, 0x20c00
	s_addc_u32 s59, s55, 0
	global_load_dwordx4 v[112:115], v3, s[58:59] nt
	global_load_dwordx4 v[116:119], v3, s[58:59] offset:16 nt
	s_add_u32 s58, s54, 0x40c00
	s_addc_u32 s59, s55, 0
	global_load_dwordx4 v[120:123], v3, s[58:59] nt
	global_load_dwordx4 v[124:127], v3, s[58:59] offset:16 nt
	s_waitcnt vmcnt(34)
	v_cvt_pk_f16_f32 v16, v16, v17
	v_cvt_pk_f16_f32 v17, v18, v19
	v_cvt_pk_f16_f32 v18, v20, v21
	v_cvt_pk_f16_f32 v19, v22, v23
	s_add_u32 s76, s44, 0x400
	s_addc_u32 s77, s45, 0
	global_store_dwordx4 v4, v[16:19], s[76:77] sc1
	s_waitcnt vmcnt(33)
	v_cvt_pk_f16_f32 v24, v24, v25
	v_cvt_pk_f16_f32 v25, v26, v27
	v_cvt_pk_f16_f32 v26, v28, v29
	v_cvt_pk_f16_f32 v27, v30, v31
	s_add_u32 s76, s44, 0x10400
	s_addc_u32 s77, s45, 0
	global_store_dwordx4 v4, v[24:27], s[76:77] sc1
	s_waitcnt vmcnt(32)
	v_cvt_pk_f16_f32 v32, v32, v33
	v_cvt_pk_f16_f32 v33, v34, v35
	v_cvt_pk_f16_f32 v34, v36, v37
	v_cvt_pk_f16_f32 v35, v38, v39
	s_add_u32 s76, s44, 0x20400
	s_addc_u32 s77, s45, 0
	global_store_dwordx4 v4, v[32:35], s[76:77] sc1
	s_waitcnt vmcnt(31)
	v_cvt_pk_f16_f32 v40, v40, v41
	v_cvt_pk_f16_f32 v41, v42, v43
	v_cvt_pk_f16_f32 v42, v44, v45
	v_cvt_pk_f16_f32 v43, v46, v47
	s_add_u32 s76, s44, 0x30400
	s_addc_u32 s77, s45, 0
	global_store_dwordx4 v4, v[40:43], s[76:77] sc1
	s_waitcnt vmcnt(30)
	v_cvt_pk_f16_f32 v48, v48, v49
	v_cvt_pk_f16_f32 v49, v50, v51
	v_cvt_pk_f16_f32 v50, v52, v53
	v_cvt_pk_f16_f32 v51, v54, v55
	s_add_u32 s76, s46, 0x400
	s_addc_u32 s77, s47, 0
	global_store_dwordx4 v4, v[48:51], s[76:77] sc1
	s_waitcnt vmcnt(29)
	v_cvt_pk_f16_f32 v56, v56, v57
	v_cvt_pk_f16_f32 v57, v58, v59
	v_cvt_pk_f16_f32 v58, v60, v61
	v_cvt_pk_f16_f32 v59, v62, v63
	s_add_u32 s76, s46, 0x10400
	s_addc_u32 s77, s47, 0
	global_store_dwordx4 v4, v[56:59], s[76:77] sc1
	s_waitcnt vmcnt(28)
	v_cvt_pk_f16_f32 v64, v64, v65
	v_cvt_pk_f16_f32 v65, v66, v67
	v_cvt_pk_f16_f32 v66, v68, v69
	v_cvt_pk_f16_f32 v67, v70, v71
	s_add_u32 s76, s46, 0x20400
	s_addc_u32 s77, s47, 0
	global_store_dwordx4 v4, v[64:67], s[76:77] sc1
	s_waitcnt vmcnt(22)
	s_barrier
	s_mov_b64 s[56:57], exec
	s_and_b64 exec, exec, s[78:79]
	global_store_dword v6, v5, s[48:49] offset:256 sc1
	s_mov_b64 exec, s[56:57]
	s_waitcnt vmcnt(20)
	v_cvt_pk_f16_f32 v72, v72, v73
	v_cvt_pk_f16_f32 v73, v74, v75
	v_cvt_pk_f16_f32 v74, v76, v77
	v_cvt_pk_f16_f32 v75, v78, v79
	s_add_u32 s76, s44, 0x600
	s_addc_u32 s77, s45, 0
	global_store_dwordx4 v4, v[72:75], s[76:77] sc1
	s_waitcnt vmcnt(19)
	v_cvt_pk_f16_f32 v80, v80, v81
	v_cvt_pk_f16_f32 v81, v82, v83
	v_cvt_pk_f16_f32 v82, v84, v85
	v_cvt_pk_f16_f32 v83, v86, v87
	s_add_u32 s76, s44, 0x10600
	s_addc_u32 s77, s45, 0
	global_store_dwordx4 v4, v[80:83], s[76:77] sc1
	s_waitcnt vmcnt(18)
	v_cvt_pk_f16_f32 v88, v88, v89
	v_cvt_pk_f16_f32 v89, v90, v91
	v_cvt_pk_f16_f32 v90, v92, v93
	v_cvt_pk_f16_f32 v91, v94, v95
	s_add_u32 s76, s44, 0x20600
	s_addc_u32 s77, s45, 0
	global_store_dwordx4 v4, v[88:91], s[76:77] sc1
	s_waitcnt vmcnt(17)
	v_cvt_pk_f16_f32 v96, v96, v97
	v_cvt_pk_f16_f32 v97, v98, v99
	v_cvt_pk_f16_f32 v98, v100, v101
	v_cvt_pk_f16_f32 v99, v102, v103
	s_add_u32 s76, s44, 0x30600
	s_addc_u32 s77, s45, 0
	global_store_dwordx4 v4, v[96:99], s[76:77] sc1
	s_waitcnt vmcnt(16)
	v_cvt_pk_f16_f32 v104, v104, v105
	v_cvt_pk_f16_f32 v105, v106, v107
	v_cvt_pk_f16_f32 v106, v108, v109
	v_cvt_pk_f16_f32 v107, v110, v111
	s_add_u32 s76, s46, 0x600
	s_addc_u32 s77, s47, 0
	global_store_dwordx4 v4, v[104:107], s[76:77] sc1
	s_waitcnt vmcnt(15)
	v_cvt_pk_f16_f32 v112, v112, v113
	v_cvt_pk_f16_f32 v113, v114, v115
	v_cvt_pk_f16_f32 v114, v116, v117
	v_cvt_pk_f16_f32 v115, v118, v119
	s_add_u32 s76, s46, 0x10600
	s_addc_u32 s77, s47, 0
	global_store_dwordx4 v4, v[112:115], s[76:77] sc1
	s_waitcnt vmcnt(14)
	v_cvt_pk_f16_f32 v120, v120, v121
	v_cvt_pk_f16_f32 v121, v122, v123
	v_cvt_pk_f16_f32 v122, v124, v125
	v_cvt_pk_f16_f32 v123, v126, v127
	s_add_u32 s76, s46, 0x20600
	s_addc_u32 s77, s47, 0
	global_store_dwordx4 v4, v[120:123], s[76:77] sc1
	s_waitcnt vmcnt(8)
	s_barrier
	s_mov_b64 s[56:57], exec
	s_and_b64 exec, exec, s[78:79]
	global_store_dword v6, v5, s[48:49] offset:512 sc1
	s_mov_b64 exec, s[56:57]
	s_waitcnt vmcnt(1)
	s_barrier
	s_mov_b64 s[56:57], exec
	s_and_b64 exec, exec, s[78:79]
	global_store_dword v6, v5, s[48:49] offset:768 sc1
	s_mov_b64 exec, s[56:57]
	s_add_i32 s24, s2, 0xffffff40
	s_lshl_b32 s20, s24, 4
	s_lshl_b32 s0, s24, 5
	s_ashr_i32 s21, s20, 31
	s_and_b32 s25, s0, 0xffffffc0
	s_lshl_b64 s[20:21], s[20:21], 2
	v_lshrrev_b32_e32 v6, 6, v0
	s_waitcnt lgkmcnt(0)
	s_add_u32 s26, s30, s20
	s_addc_u32 s27, s31, s21
	v_lshl_or_b32 v2, v6, 3, s25
	s_and_b32 s25, s2, 1
	s_lshl_b32 s2, s25, 7
	s_add_u32 s20, s28, s2
	v_and_b32_e32 v7, 63, v0
	s_mov_b32 s3, 0
	s_addc_u32 s21, s29, 0
	s_bfe_u32 s2, s24, 0x1a0001
	v_add_u32_e32 v2, v2, v7
	v_mov_b32_e32 v3, 0
	s_lshl_b64 s[2:3], s[2:3], 19
	v_lshl_add_u32 v1, v6, 2, 0
	v_lshlrev_b64 v[4:5], 8, v[2:3]
	v_lshl_or_b32 v2, v6, 16, s2
	s_lshl_b32 s2, s25, 12
	v_lshlrev_b32_e32 v6, 2, v7
	v_cmp_gt_u32_e64 s[0:1], 8, v7
	v_cmp_eq_u32_e64 s[22:23], 0, v7
	v_cmp_eq_u32_e64 s[6:7], 1, v7
	v_cmp_eq_u32_e64 s[8:9], 2, v7
	v_cmp_eq_u32_e64 s[10:11], 3, v7
	v_cmp_eq_u32_e64 s[12:13], 4, v7
	v_cmp_eq_u32_e64 s[14:15], 5, v7
	v_cmp_eq_u32_e64 s[16:17], 6, v7
	v_cmp_eq_u32_e64 s[18:19], 7, v7
	v_or3_b32 v6, v2, s2, v6
	v_mov_b32_e32 v7, s3
	v_cmp_eq_u32_e64 s[4:5], 0, v0
	v_lshl_add_u64 v[4:5], s[20:21], 0, v[4:5]
	v_lshl_add_u64 v[6:7], s[42:43], 0, v[6:7]
	s_mov_b64 s[28:29], 0
	s_lshr_b32 s58, s24, 1
	s_lshl_b32 s58, s58, 19
	s_add_u32 s60, s42, s58
	s_addc_u32 s61, s43, 0
	s_add_u32 s62, s60, 0x2000
	s_addc_u32 s63, s61, 0
	s_add_u32 s64, s62, 0x2000
	s_addc_u32 s65, s63, 0
	s_add_u32 s66, s64, 0x2000
	s_addc_u32 s67, s65, 0
	s_add_u32 s68, s66, 0x2000
	s_addc_u32 s69, s67, 0
	s_add_u32 s70, s68, 0x2000
	s_addc_u32 s71, s69, 0
	s_add_u32 s72, s70, 0x2000
	s_addc_u32 s73, s71, 0
	s_add_u32 s74, s72, 0x2000
	s_addc_u32 s75, s73, 0
	v_lshrrev_b32_e32 v96, 6, v0
	v_lshlrev_b32_e32 v96, 16, v96
	v_and_b32_e32 v97, 63, v0
	v_lshl_add_u32 v96, v97, 2, v96
	s_and_b32 s59, s24, 1
	s_lshl_b32 s59, s59, 12
	v_add_u32_e32 v96, s59, v96
	s_mov_b32 s76, 0
	s_mov_b32 s77, 0
	global_load_dword v100, v96, s[60:61] offset:0 nt
	global_load_dword v101, v96, s[62:63] offset:0 nt
	global_load_dword v102, v96, s[64:65] offset:0 nt
	global_load_dword v103, v96, s[66:67] offset:0 nt
	global_load_dword v104, v96, s[68:69] offset:0 nt
	global_load_dword v105, v96, s[70:71] offset:0 nt
	global_load_dword v106, v96, s[72:73] offset:0 nt
	global_load_dword v107, v96, s[74:75] offset:0 nt
	global_load_dword v108, v96, s[60:61] offset:256 nt
	global_load_dword v109, v96, s[62:63] offset:256 nt
	global_load_dword v110, v96, s[64:65] offset:256 nt
	global_load_dword v111, v96, s[66:67] offset:256 nt
	global_load_dword v112, v96, s[68:69] offset:256 nt
	global_load_dword v113, v96, s[70:71] offset:256 nt
	global_load_dword v114, v96, s[72:73] offset:256 nt
	global_load_dword v115, v96, s[74:75] offset:256 nt
	global_load_dword v116, v96, s[60:61] offset:512 nt
	global_load_dword v117, v96, s[62:63] offset:512 nt
	global_load_dword v118, v96, s[64:65] offset:512 nt
	global_load_dword v119, v96, s[66:67] offset:512 nt
	global_load_dword v120, v96, s[68:69] offset:512 nt
	global_load_dword v121, v96, s[70:71] offset:512 nt
	global_load_dword v122, v96, s[72:73] offset:512 nt
	global_load_dword v123, v96, s[74:75] offset:512 nt
	global_load_dword v124, v96, s[60:61] offset:768 nt
	global_load_dword v125, v96, s[62:63] offset:768 nt
	global_load_dword v126, v96, s[64:65] offset:768 nt
	global_load_dword v127, v96, s[66:67] offset:768 nt
	global_load_dword v128, v96, s[68:69] offset:768 nt
	global_load_dword v129, v96, s[70:71] offset:768 nt
	global_load_dword v130, v96, s[72:73] offset:768 nt
	global_load_dword v131, v96, s[74:75] offset:768 nt
	global_load_dword v132, v96, s[60:61] offset:1024 nt
	global_load_dword v133, v96, s[62:63] offset:1024 nt
	global_load_dword v134, v96, s[64:65] offset:1024 nt
	global_load_dword v135, v96, s[66:67] offset:1024 nt
	global_load_dword v136, v96, s[68:69] offset:1024 nt
	global_load_dword v137, v96, s[70:71] offset:1024 nt
	global_load_dword v138, v96, s[72:73] offset:1024 nt
	global_load_dword v139, v96, s[74:75] offset:1024 nt
	global_load_dword v140, v96, s[60:61] offset:1280 nt
	global_load_dword v141, v96, s[62:63] offset:1280 nt
	global_load_dword v142, v96, s[64:65] offset:1280 nt
	global_load_dword v143, v96, s[66:67] offset:1280 nt
	global_load_dword v144, v96, s[68:69] offset:1280 nt
	global_load_dword v145, v96, s[70:71] offset:1280 nt
	global_load_dword v146, v96, s[72:73] offset:1280 nt
	global_load_dword v147, v96, s[74:75] offset:1280 nt
	global_load_dword v148, v96, s[60:61] offset:1536 nt
	global_load_dword v149, v96, s[62:63] offset:1536 nt
	global_load_dword v150, v96, s[64:65] offset:1536 nt
	global_load_dword v151, v96, s[66:67] offset:1536 nt
	global_load_dword v152, v96, s[68:69] offset:1536 nt
	global_load_dword v153, v96, s[70:71] offset:1536 nt
	global_load_dword v154, v96, s[72:73] offset:1536 nt
	global_load_dword v155, v96, s[74:75] offset:1536 nt
	s_waitcnt vmcnt(48)
	v_cmp_ne_u32_e32 vcc, 0, v100
	s_nop 1
	v_mov_b32_e32 v2, vcc_lo
	v_mov_b32_e32 v9, vcc_hi
	v_cmp_ne_u32_e32 vcc, 0, v101
	v_cndmask_b32_e64 v2, 0, v2, s[22:23]
	v_cndmask_b32_e64 v9, 0, v9, s[22:23]
	v_mov_b32_e32 v11, vcc_hi
	v_mov_b32_e32 v14, vcc_lo
	v_cndmask_b32_e64 v9, v9, v11, s[6:7]
	v_cndmask_b32_e64 v2, v2, v14, s[6:7]
	v_cmp_ne_u32_e32 vcc, 0, v102
	s_nop 1
	v_mov_b32_e32 v11, vcc_lo
	v_mov_b32_e32 v14, vcc_hi
	v_cmp_ne_u32_e32 vcc, 0, v103
	v_cndmask_b32_e64 v2, v2, v11, s[8:9]
	v_cndmask_b32_e64 v9, v9, v14, s[8:9]
	v_mov_b32_e32 v11, vcc_hi
	v_mov_b32_e32 v14, vcc_lo
	v_cmp_ne_u32_e32 vcc, 0, v104
	v_cndmask_b32_e64 v9, v9, v11, s[10:11]
	v_cndmask_b32_e64 v2, v2, v14, s[10:11]
	v_mov_b32_e32 v11, vcc_lo
	v_mov_b32_e32 v12, vcc_hi
	v_cmp_ne_u32_e32 vcc, 0, v105
	v_cndmask_b32_e64 v2, v2, v11, s[12:13]
	v_cndmask_b32_e64 v9, v9, v12, s[12:13]
	v_mov_b32_e32 v11, vcc_hi
	v_mov_b32_e32 v12, vcc_lo
	v_cndmask_b32_e64 v9, v9, v11, s[14:15]
	v_cndmask_b32_e64 v2, v2, v12, s[14:15]
	v_cmp_ne_u32_e32 vcc, 0, v106
	s_nop 1
	v_mov_b32_e32 v10, vcc_lo
	v_mov_b32_e32 v11, vcc_hi
	v_cmp_ne_u32_e32 vcc, 0, v107
	v_cndmask_b32_e64 v2, v2, v10, s[16:17]
	v_cndmask_b32_e64 v8, v9, v11, s[16:17]
	v_mov_b32_e32 v9, vcc_hi
	v_mov_b32_e32 v10, vcc_lo
	v_cndmask_b32_e64 v9, v8, v9, s[18:19]
	v_cndmask_b32_e64 v8, v2, v10, s[18:19]
	s_mov_b64 s[2:3], exec
	s_mov_b64 exec, s[0:1]
	global_store_dwordx2 v[4:5], v[8:9], off
	s_mov_b64 exec, s[2:3]
	v_cmp_ne_u64_e32 vcc, 0, v[8:9]
	s_and_b64 s[20:21], s[0:1], vcc
	s_cmp_lg_u64 s[20:21], 0
	s_cselect_b32 s20, 1, 0
	s_or_b32 s76, s76, s20
	v_cmp_ne_u64_e32 vcc, -1, v[8:9]
	s_and_b64 s[20:21], s[0:1], vcc
	s_cmp_lg_u64 s[20:21], 0
	s_cselect_b32 s20, 1, 0
	s_or_b32 s77, s77, s20
	v_lshl_add_u64 v[4:5], v[4:5], 0, 8
	global_load_dword v156, v96, s[60:61] offset:1792 nt
	global_load_dword v157, v96, s[62:63] offset:1792 nt
	global_load_dword v158, v96, s[64:65] offset:1792 nt
	global_load_dword v159, v96, s[66:67] offset:1792 nt
	global_load_dword v160, v96, s[68:69] offset:1792 nt
	global_load_dword v161, v96, s[70:71] offset:1792 nt
	global_load_dword v162, v96, s[72:73] offset:1792 nt
	global_load_dword v163, v96, s[74:75] offset:1792 nt
	s_waitcnt vmcnt(49)
	v_cmp_ne_u32_e32 vcc, 0, v108
	s_nop 1
	v_mov_b32_e32 v2, vcc_lo
	v_mov_b32_e32 v9, vcc_hi
	v_cmp_ne_u32_e32 vcc, 0, v109
	v_cndmask_b32_e64 v2, 0, v2, s[22:23]
	v_cndmask_b32_e64 v9, 0, v9, s[22:23]
	v_mov_b32_e32 v11, vcc_hi
	v_mov_b32_e32 v14, vcc_lo
	v_cndmask_b32_e64 v9, v9, v11, s[6:7]
	v_cndmask_b32_e64 v2, v2, v14, s[6:7]
	v_cmp_ne_u32_e32 vcc, 0, v110
	s_nop 1
	v_mov_b32_e32 v11, vcc_lo
	v_mov_b32_e32 v14, vcc_hi
	v_cmp_ne_u32_e32 vcc, 0, v111
	v_cndmask_b32_e64 v2, v2, v11, s[8:9]
	v_cndmask_b32_e64 v9, v9, v14, s[8:9]
	v_mov_b32_e32 v11, vcc_hi
	v_mov_b32_e32 v14, vcc_lo
	v_cmp_ne_u32_e32 vcc, 0, v112
	v_cndmask_b32_e64 v9, v9, v11, s[10:11]
	v_cndmask_b32_e64 v2, v2, v14, s[10:11]
	v_mov_b32_e32 v11, vcc_lo
	v_mov_b32_e32 v12, vcc_hi
	v_cmp_ne_u32_e32 vcc, 0, v113
	v_cndmask_b32_e64 v2, v2, v11, s[12:13]
	v_cndmask_b32_e64 v9, v9, v12, s[12:13]
	v_mov_b32_e32 v11, vcc_hi
	v_mov_b32_e32 v12, vcc_lo
	v_cndmask_b32_e64 v9, v9, v11, s[14:15]
	v_cndmask_b32_e64 v2, v2, v12, s[14:15]
	v_cmp_ne_u32_e32 vcc, 0, v114
	s_nop 1
	v_mov_b32_e32 v10, vcc_lo
	v_mov_b32_e32 v11, vcc_hi
	v_cmp_ne_u32_e32 vcc, 0, v115
	v_cndmask_b32_e64 v2, v2, v10, s[16:17]
	v_cndmask_b32_e64 v8, v9, v11, s[16:17]
	v_mov_b32_e32 v9, vcc_hi
	v_mov_b32_e32 v10, vcc_lo
	v_cndmask_b32_e64 v9, v8, v9, s[18:19]
	v_cndmask_b32_e64 v8, v2, v10, s[18:19]
	s_mov_b64 s[2:3], exec
	s_mov_b64 exec, s[0:1]
	global_store_dwordx2 v[4:5], v[8:9], off
	s_mov_b64 exec, s[2:3]
	v_cmp_ne_u64_e32 vcc, 0, v[8:9]
	s_and_b64 s[20:21], s[0:1], vcc
	s_cmp_lg_u64 s[20:21], 0
	s_cselect_b32 s20, 2, 0
	s_or_b32 s76, s76, s20
	v_cmp_ne_u64_e32 vcc, -1, v[8:9]
	s_and_b64 s[20:21], s[0:1], vcc
	s_cmp_lg_u64 s[20:21], 0
	s_cselect_b32 s20, 2, 0
	s_or_b32 s77, s77, s20
	v_lshl_add_u64 v[4:5], v[4:5], 0, 8
	global_load_dword v164, v96, s[60:61] offset:2048 nt
	global_load_dword v165, v96, s[62:63] offset:2048 nt
	global_load_dword v166, v96, s[64:65] offset:2048 nt
	global_load_dword v167, v96, s[66:67] offset:2048 nt
	global_load_dword v168, v96, s[68:69] offset:2048 nt
	global_load_dword v169, v96, s[70:71] offset:2048 nt
	global_load_dword v170, v96, s[72:73] offset:2048 nt
	global_load_dword v171, v96, s[74:75] offset:2048 nt
	s_waitcnt vmcnt(50)
	v_cmp_ne_u32_e32 vcc, 0, v116
	s_nop 1
	v_mov_b32_e32 v2, vcc_lo
	v_mov_b32_e32 v9, vcc_hi
	v_cmp_ne_u32_e32 vcc, 0, v117
	v_cndmask_b32_e64 v2, 0, v2, s[22:23]
	v_cndmask_b32_e64 v9, 0, v9, s[22:23]
	v_mov_b32_e32 v11, vcc_hi
	v_mov_b32_e32 v14, vcc_lo
	v_cndmask_b32_e64 v9, v9, v11, s[6:7]
	v_cndmask_b32_e64 v2, v2, v14, s[6:7]
	v_cmp_ne_u32_e32 vcc, 0, v118
	s_nop 1
	v_mov_b32_e32 v11, vcc_lo
	v_mov_b32_e32 v14, vcc_hi
	v_cmp_ne_u32_e32 vcc, 0, v119
	v_cndmask_b32_e64 v2, v2, v11, s[8:9]
	v_cndmask_b32_e64 v9, v9, v14, s[8:9]
	v_mov_b32_e32 v11, vcc_hi
	v_mov_b32_e32 v14, vcc_lo
	v_cmp_ne_u32_e32 vcc, 0, v120
	v_cndmask_b32_e64 v9, v9, v11, s[10:11]
	v_cndmask_b32_e64 v2, v2, v14, s[10:11]
	v_mov_b32_e32 v11, vcc_lo
	v_mov_b32_e32 v12, vcc_hi
	v_cmp_ne_u32_e32 vcc, 0, v121
	v_cndmask_b32_e64 v2, v2, v11, s[12:13]
	v_cndmask_b32_e64 v9, v9, v12, s[12:13]
	v_mov_b32_e32 v11, vcc_hi
	v_mov_b32_e32 v12, vcc_lo
	v_cndmask_b32_e64 v9, v9, v11, s[14:15]
	v_cndmask_b32_e64 v2, v2, v12, s[14:15]
	v_cmp_ne_u32_e32 vcc, 0, v122
	s_nop 1
	v_mov_b32_e32 v10, vcc_lo
	v_mov_b32_e32 v11, vcc_hi
	v_cmp_ne_u32_e32 vcc, 0, v123
	v_cndmask_b32_e64 v2, v2, v10, s[16:17]
	v_cndmask_b32_e64 v8, v9, v11, s[16:17]
	v_mov_b32_e32 v9, vcc_hi
	v_mov_b32_e32 v10, vcc_lo
	v_cndmask_b32_e64 v9, v8, v9, s[18:19]
	v_cndmask_b32_e64 v8, v2, v10, s[18:19]
	s_mov_b64 s[2:3], exec
	s_mov_b64 exec, s[0:1]
	global_store_dwordx2 v[4:5], v[8:9], off
	s_mov_b64 exec, s[2:3]
	v_cmp_ne_u64_e32 vcc, 0, v[8:9]
	s_and_b64 s[20:21], s[0:1], vcc
	s_cmp_lg_u64 s[20:21], 0
	s_cselect_b32 s20, 4, 0
	s_or_b32 s76, s76, s20
	v_cmp_ne_u64_e32 vcc, -1, v[8:9]
	s_and_b64 s[20:21], s[0:1], vcc
	s_cmp_lg_u64 s[20:21], 0
	s_cselect_b32 s20, 4, 0
	s_or_b32 s77, s77, s20
	v_lshl_add_u64 v[4:5], v[4:5], 0, 8
	global_load_dword v172, v96, s[60:61] offset:2304 nt
	global_load_dword v173, v96, s[62:63] offset:2304 nt
	global_load_dword v174, v96, s[64:65] offset:2304 nt
	global_load_dword v175, v96, s[66:67] offset:2304 nt
	global_load_dword v176, v96, s[68:69] offset:2304 nt
	global_load_dword v177, v96, s[70:71] offset:2304 nt
	global_load_dword v178, v96, s[72:73] offset:2304 nt
	global_load_dword v179, v96, s[74:75] offset:2304 nt
	s_waitcnt vmcnt(51)
	v_cmp_ne_u32_e32 vcc, 0, v124
	s_nop 1
	v_mov_b32_e32 v2, vcc_lo
	v_mov_b32_e32 v9, vcc_hi
	v_cmp_ne_u32_e32 vcc, 0, v125
	v_cndmask_b32_e64 v2, 0, v2, s[22:23]
	v_cndmask_b32_e64 v9, 0, v9, s[22:23]
	v_mov_b32_e32 v11, vcc_hi
	v_mov_b32_e32 v14, vcc_lo
	v_cndmask_b32_e64 v9, v9, v11, s[6:7]
	v_cndmask_b32_e64 v2, v2, v14, s[6:7]
	v_cmp_ne_u32_e32 vcc, 0, v126
	s_nop 1
	v_mov_b32_e32 v11, vcc_lo
	v_mov_b32_e32 v14, vcc_hi
	v_cmp_ne_u32_e32 vcc, 0, v127
	v_cndmask_b32_e64 v2, v2, v11, s[8:9]
	v_cndmask_b32_e64 v9, v9, v14, s[8:9]
	v_mov_b32_e32 v11, vcc_hi
	v_mov_b32_e32 v14, vcc_lo
	v_cmp_ne_u32_e32 vcc, 0, v128
	v_cndmask_b32_e64 v9, v9, v11, s[10:11]
	v_cndmask_b32_e64 v2, v2, v14, s[10:11]
	v_mov_b32_e32 v11, vcc_lo
	v_mov_b32_e32 v12, vcc_hi
	v_cmp_ne_u32_e32 vcc, 0, v129
	v_cndmask_b32_e64 v2, v2, v11, s[12:13]
	v_cndmask_b32_e64 v9, v9, v12, s[12:13]
	v_mov_b32_e32 v11, vcc_hi
	v_mov_b32_e32 v12, vcc_lo
	v_cndmask_b32_e64 v9, v9, v11, s[14:15]
	v_cndmask_b32_e64 v2, v2, v12, s[14:15]
	v_cmp_ne_u32_e32 vcc, 0, v130
	s_nop 1
	v_mov_b32_e32 v10, vcc_lo
	v_mov_b32_e32 v11, vcc_hi
	v_cmp_ne_u32_e32 vcc, 0, v131
	v_cndmask_b32_e64 v2, v2, v10, s[16:17]
	v_cndmask_b32_e64 v8, v9, v11, s[16:17]
	v_mov_b32_e32 v9, vcc_hi
	v_mov_b32_e32 v10, vcc_lo
	v_cndmask_b32_e64 v9, v8, v9, s[18:19]
	v_cndmask_b32_e64 v8, v2, v10, s[18:19]
	s_mov_b64 s[2:3], exec
	s_mov_b64 exec, s[0:1]
	global_store_dwordx2 v[4:5], v[8:9], off
	s_mov_b64 exec, s[2:3]
	v_cmp_ne_u64_e32 vcc, 0, v[8:9]
	s_and_b64 s[20:21], s[0:1], vcc
	s_cmp_lg_u64 s[20:21], 0
	s_cselect_b32 s20, 8, 0
	s_or_b32 s76, s76, s20
	v_cmp_ne_u64_e32 vcc, -1, v[8:9]
	s_and_b64 s[20:21], s[0:1], vcc
	s_cmp_lg_u64 s[20:21], 0
	s_cselect_b32 s20, 8, 0
	s_or_b32 s77, s77, s20
	v_lshl_add_u64 v[4:5], v[4:5], 0, 8
	global_load_dword v180, v96, s[60:61] offset:2560 nt
	global_load_dword v181, v96, s[62:63] offset:2560 nt
	global_load_dword v182, v96, s[64:65] offset:2560 nt
	global_load_dword v183, v96, s[66:67] offset:2560 nt
	global_load_dword v184, v96, s[68:69] offset:2560 nt
	global_load_dword v185, v96, s[70:71] offset:2560 nt
	global_load_dword v186, v96, s[72:73] offset:2560 nt
	global_load_dword v187, v96, s[74:75] offset:2560 nt
	s_waitcnt vmcnt(52)
	v_cmp_ne_u32_e32 vcc, 0, v132
	s_nop 1
	v_mov_b32_e32 v2, vcc_lo
	v_mov_b32_e32 v9, vcc_hi
	v_cmp_ne_u32_e32 vcc, 0, v133
	v_cndmask_b32_e64 v2, 0, v2, s[22:23]
	v_cndmask_b32_e64 v9, 0, v9, s[22:23]
	v_mov_b32_e32 v11, vcc_hi
	v_mov_b32_e32 v14, vcc_lo
	v_cndmask_b32_e64 v9, v9, v11, s[6:7]
	v_cndmask_b32_e64 v2, v2, v14, s[6:7]
	v_cmp_ne_u32_e32 vcc, 0, v134
	s_nop 1
	v_mov_b32_e32 v11, vcc_lo
	v_mov_b32_e32 v14, vcc_hi
	v_cmp_ne_u32_e32 vcc, 0, v135
	v_cndmask_b32_e64 v2, v2, v11, s[8:9]
	v_cndmask_b32_e64 v9, v9, v14, s[8:9]
	v_mov_b32_e32 v11, vcc_hi
	v_mov_b32_e32 v14, vcc_lo
	v_cmp_ne_u32_e32 vcc, 0, v136
	v_cndmask_b32_e64 v9, v9, v11, s[10:11]
	v_cndmask_b32_e64 v2, v2, v14, s[10:11]
	v_mov_b32_e32 v11, vcc_lo
	v_mov_b32_e32 v12, vcc_hi
	v_cmp_ne_u32_e32 vcc, 0, v137
	v_cndmask_b32_e64 v2, v2, v11, s[12:13]
	v_cndmask_b32_e64 v9, v9, v12, s[12:13]
	v_mov_b32_e32 v11, vcc_hi
	v_mov_b32_e32 v12, vcc_lo
	v_cndmask_b32_e64 v9, v9, v11, s[14:15]
	v_cndmask_b32_e64 v2, v2, v12, s[14:15]
	v_cmp_ne_u32_e32 vcc, 0, v138
	s_nop 1
	v_mov_b32_e32 v10, vcc_lo
	v_mov_b32_e32 v11, vcc_hi
	v_cmp_ne_u32_e32 vcc, 0, v139
	v_cndmask_b32_e64 v2, v2, v10, s[16:17]
	v_cndmask_b32_e64 v8, v9, v11, s[16:17]
	v_mov_b32_e32 v9, vcc_hi
	v_mov_b32_e32 v10, vcc_lo
	v_cndmask_b32_e64 v9, v8, v9, s[18:19]
	v_cndmask_b32_e64 v8, v2, v10, s[18:19]
	s_mov_b64 s[2:3], exec
	s_mov_b64 exec, s[0:1]
	global_store_dwordx2 v[4:5], v[8:9], off
	s_mov_b64 exec, s[2:3]
	v_cmp_ne_u64_e32 vcc, 0, v[8:9]
	s_and_b64 s[20:21], s[0:1], vcc
	s_cmp_lg_u64 s[20:21], 0
	s_cselect_b32 s20, 16, 0
	s_or_b32 s76, s76, s20
	v_cmp_ne_u64_e32 vcc, -1, v[8:9]
	s_and_b64 s[20:21], s[0:1], vcc
	s_cmp_lg_u64 s[20:21], 0
	s_cselect_b32 s20, 16, 0
	s_or_b32 s77, s77, s20
	v_lshl_add_u64 v[4:5], v[4:5], 0, 8
	global_load_dword v188, v96, s[60:61] offset:2816 nt
	global_load_dword v189, v96, s[62:63] offset:2816 nt
	global_load_dword v190, v96, s[64:65] offset:2816 nt
	global_load_dword v191, v96, s[66:67] offset:2816 nt
	global_load_dword v192, v96, s[68:69] offset:2816 nt
	global_load_dword v193, v96, s[70:71] offset:2816 nt
	global_load_dword v194, v96, s[72:73] offset:2816 nt
	global_load_dword v195, v96, s[74:75] offset:2816 nt
	s_waitcnt vmcnt(53)
	v_cmp_ne_u32_e32 vcc, 0, v140
	s_nop 1
	v_mov_b32_e32 v2, vcc_lo
	v_mov_b32_e32 v9, vcc_hi
	v_cmp_ne_u32_e32 vcc, 0, v141
	v_cndmask_b32_e64 v2, 0, v2, s[22:23]
	v_cndmask_b32_e64 v9, 0, v9, s[22:23]
	v_mov_b32_e32 v11, vcc_hi
	v_mov_b32_e32 v14, vcc_lo
	v_cndmask_b32_e64 v9, v9, v11, s[6:7]
	v_cndmask_b32_e64 v2, v2, v14, s[6:7]
	v_cmp_ne_u32_e32 vcc, 0, v142
	s_nop 1
	v_mov_b32_e32 v11, vcc_lo
	v_mov_b32_e32 v14, vcc_hi
	v_cmp_ne_u32_e32 vcc, 0, v143
	v_cndmask_b32_e64 v2, v2, v11, s[8:9]
	v_cndmask_b32_e64 v9, v9, v14, s[8:9]
	v_mov_b32_e32 v11, vcc_hi
	v_mov_b32_e32 v14, vcc_lo
	v_cmp_ne_u32_e32 vcc, 0, v144
	v_cndmask_b32_e64 v9, v9, v11, s[10:11]
	v_cndmask_b32_e64 v2, v2, v14, s[10:11]
	v_mov_b32_e32 v11, vcc_lo
	v_mov_b32_e32 v12, vcc_hi
	v_cmp_ne_u32_e32 vcc, 0, v145
	v_cndmask_b32_e64 v2, v2, v11, s[12:13]
	v_cndmask_b32_e64 v9, v9, v12, s[12:13]
	v_mov_b32_e32 v11, vcc_hi
	v_mov_b32_e32 v12, vcc_lo
	v_cndmask_b32_e64 v9, v9, v11, s[14:15]
	v_cndmask_b32_e64 v2, v2, v12, s[14:15]
	v_cmp_ne_u32_e32 vcc, 0, v146
	s_nop 1
	v_mov_b32_e32 v10, vcc_lo
	v_mov_b32_e32 v11, vcc_hi
	v_cmp_ne_u32_e32 vcc, 0, v147
	v_cndmask_b32_e64 v2, v2, v10, s[16:17]
	v_cndmask_b32_e64 v8, v9, v11, s[16:17]
	v_mov_b32_e32 v9, vcc_hi
	v_mov_b32_e32 v10, vcc_lo
	v_cndmask_b32_e64 v9, v8, v9, s[18:19]
	v_cndmask_b32_e64 v8, v2, v10, s[18:19]
	s_mov_b64 s[2:3], exec
	s_mov_b64 exec, s[0:1]
	global_store_dwordx2 v[4:5], v[8:9], off
	s_mov_b64 exec, s[2:3]
	v_cmp_ne_u64_e32 vcc, 0, v[8:9]
	s_and_b64 s[20:21], s[0:1], vcc
	s_cmp_lg_u64 s[20:21], 0
	s_cselect_b32 s20, 32, 0
	s_or_b32 s76, s76, s20
	v_cmp_ne_u64_e32 vcc, -1, v[8:9]
	s_and_b64 s[20:21], s[0:1], vcc
	s_cmp_lg_u64 s[20:21], 0
	s_cselect_b32 s20, 32, 0
	s_or_b32 s77, s77, s20
	v_lshl_add_u64 v[4:5], v[4:5], 0, 8
	global_load_dword v196, v96, s[60:61] offset:3072 nt
	global_load_dword v197, v96, s[62:63] offset:3072 nt
	global_load_dword v198, v96, s[64:65] offset:3072 nt
	global_load_dword v199, v96, s[66:67] offset:3072 nt
	global_load_dword v200, v96, s[68:69] offset:3072 nt
	global_load_dword v201, v96, s[70:71] offset:3072 nt
	global_load_dword v202, v96, s[72:73] offset:3072 nt
	global_load_dword v203, v96, s[74:75] offset:3072 nt
	s_waitcnt vmcnt(54)
	v_cmp_ne_u32_e32 vcc, 0, v148
	s_nop 1
	v_mov_b32_e32 v2, vcc_lo
	v_mov_b32_e32 v9, vcc_hi
	v_cmp_ne_u32_e32 vcc, 0, v149
	v_cndmask_b32_e64 v2, 0, v2, s[22:23]
	v_cndmask_b32_e64 v9, 0, v9, s[22:23]
	v_mov_b32_e32 v11, vcc_hi
	v_mov_b32_e32 v14, vcc_lo
	v_cndmask_b32_e64 v9, v9, v11, s[6:7]
	v_cndmask_b32_e64 v2, v2, v14, s[6:7]
	v_cmp_ne_u32_e32 vcc, 0, v150
	s_nop 1
	v_mov_b32_e32 v11, vcc_lo
	v_mov_b32_e32 v14, vcc_hi
	v_cmp_ne_u32_e32 vcc, 0, v151
	v_cndmask_b32_e64 v2, v2, v11, s[8:9]
	v_cndmask_b32_e64 v9, v9, v14, s[8:9]
	v_mov_b32_e32 v11, vcc_hi
	v_mov_b32_e32 v14, vcc_lo
	v_cmp_ne_u32_e32 vcc, 0, v152
	v_cndmask_b32_e64 v9, v9, v11, s[10:11]
	v_cndmask_b32_e64 v2, v2, v14, s[10:11]
	v_mov_b32_e32 v11, vcc_lo
	v_mov_b32_e32 v12, vcc_hi
	v_cmp_ne_u32_e32 vcc, 0, v153
	v_cndmask_b32_e64 v2, v2, v11, s[12:13]
	v_cndmask_b32_e64 v9, v9, v12, s[12:13]
	v_mov_b32_e32 v11, vcc_hi
	v_mov_b32_e32 v12, vcc_lo
	v_cndmask_b32_e64 v9, v9, v11, s[14:15]
	v_cndmask_b32_e64 v2, v2, v12, s[14:15]
	v_cmp_ne_u32_e32 vcc, 0, v154
	s_nop 1
	v_mov_b32_e32 v10, vcc_lo
	v_mov_b32_e32 v11, vcc_hi
	v_cmp_ne_u32_e32 vcc, 0, v155
	v_cndmask_b32_e64 v2, v2, v10, s[16:17]
	v_cndmask_b32_e64 v8, v9, v11, s[16:17]
	v_mov_b32_e32 v9, vcc_hi
	v_mov_b32_e32 v10, vcc_lo
	v_cndmask_b32_e64 v9, v8, v9, s[18:19]
	v_cndmask_b32_e64 v8, v2, v10, s[18:19]
	s_mov_b64 s[2:3], exec
	s_mov_b64 exec, s[0:1]
	global_store_dwordx2 v[4:5], v[8:9], off
	s_mov_b64 exec, s[2:3]
	v_cmp_ne_u64_e32 vcc, 0, v[8:9]
	s_and_b64 s[20:21], s[0:1], vcc
	s_cmp_lg_u64 s[20:21], 0
	s_cselect_b32 s20, 64, 0
	s_or_b32 s76, s76, s20
	v_cmp_ne_u64_e32 vcc, -1, v[8:9]
	s_and_b64 s[20:21], s[0:1], vcc
	s_cmp_lg_u64 s[20:21], 0
	s_cselect_b32 s20, 64, 0
	s_or_b32 s77, s77, s20
	v_lshl_add_u64 v[4:5], v[4:5], 0, 8
	global_load_dword v204, v96, s[60:61] offset:3328 nt
	global_load_dword v205, v96, s[62:63] offset:3328 nt
	global_load_dword v206, v96, s[64:65] offset:3328 nt
	global_load_dword v207, v96, s[66:67] offset:3328 nt
	global_load_dword v208, v96, s[68:69] offset:3328 nt
	global_load_dword v209, v96, s[70:71] offset:3328 nt
	global_load_dword v210, v96, s[72:73] offset:3328 nt
	global_load_dword v211, v96, s[74:75] offset:3328 nt
	s_waitcnt vmcnt(54)
	v_cmp_ne_u32_e32 vcc, 0, v156
	s_nop 1
	v_mov_b32_e32 v2, vcc_lo
	v_mov_b32_e32 v9, vcc_hi
	v_cmp_ne_u32_e32 vcc, 0, v157
	v_cndmask_b32_e64 v2, 0, v2, s[22:23]
	v_cndmask_b32_e64 v9, 0, v9, s[22:23]
	v_mov_b32_e32 v11, vcc_hi
	v_mov_b32_e32 v14, vcc_lo
	v_cndmask_b32_e64 v9, v9, v11, s[6:7]
	v_cndmask_b32_e64 v2, v2, v14, s[6:7]
	v_cmp_ne_u32_e32 vcc, 0, v158
	s_nop 1
	v_mov_b32_e32 v11, vcc_lo
	v_mov_b32_e32 v14, vcc_hi
	v_cmp_ne_u32_e32 vcc, 0, v159
	v_cndmask_b32_e64 v2, v2, v11, s[8:9]
	v_cndmask_b32_e64 v9, v9, v14, s[8:9]
	v_mov_b32_e32 v11, vcc_hi
	v_mov_b32_e32 v14, vcc_lo
	v_cmp_ne_u32_e32 vcc, 0, v160
	v_cndmask_b32_e64 v9, v9, v11, s[10:11]
	v_cndmask_b32_e64 v2, v2, v14, s[10:11]
	v_mov_b32_e32 v11, vcc_lo
	v_mov_b32_e32 v12, vcc_hi
	v_cmp_ne_u32_e32 vcc, 0, v161
	v_cndmask_b32_e64 v2, v2, v11, s[12:13]
	v_cndmask_b32_e64 v9, v9, v12, s[12:13]
	v_mov_b32_e32 v11, vcc_hi
	v_mov_b32_e32 v12, vcc_lo
	v_cndmask_b32_e64 v9, v9, v11, s[14:15]
	v_cndmask_b32_e64 v2, v2, v12, s[14:15]
	v_cmp_ne_u32_e32 vcc, 0, v162
	s_nop 1
	v_mov_b32_e32 v10, vcc_lo
	v_mov_b32_e32 v11, vcc_hi
	v_cmp_ne_u32_e32 vcc, 0, v163
	v_cndmask_b32_e64 v2, v2, v10, s[16:17]
	v_cndmask_b32_e64 v8, v9, v11, s[16:17]
	v_mov_b32_e32 v9, vcc_hi
	v_mov_b32_e32 v10, vcc_lo
	v_cndmask_b32_e64 v9, v8, v9, s[18:19]
	v_cndmask_b32_e64 v8, v2, v10, s[18:19]
	s_mov_b64 s[2:3], exec
	s_mov_b64 exec, s[0:1]
	global_store_dwordx2 v[4:5], v[8:9], off
	s_mov_b64 exec, s[2:3]
	v_cmp_ne_u64_e32 vcc, 0, v[8:9]
	s_and_b64 s[20:21], s[0:1], vcc
	s_cmp_lg_u64 s[20:21], 0
	s_cselect_b32 s20, 128, 0
	s_or_b32 s76, s76, s20
	v_cmp_ne_u64_e32 vcc, -1, v[8:9]
	s_and_b64 s[20:21], s[0:1], vcc
	s_cmp_lg_u64 s[20:21], 0
	s_cselect_b32 s20, 128, 0
	s_or_b32 s77, s77, s20
	v_lshl_add_u64 v[4:5], v[4:5], 0, 8
	global_load_dword v212, v96, s[60:61] offset:3584 nt
	global_load_dword v213, v96, s[62:63] offset:3584 nt
	global_load_dword v214, v96, s[64:65] offset:3584 nt
	global_load_dword v215, v96, s[66:67] offset:3584 nt
	global_load_dword v216, v96, s[68:69] offset:3584 nt
	global_load_dword v217, v96, s[70:71] offset:3584 nt
	global_load_dword v218, v96, s[72:73] offset:3584 nt
	global_load_dword v219, v96, s[74:75] offset:3584 nt
	s_waitcnt vmcnt(54)
	v_cmp_ne_u32_e32 vcc, 0, v164
	s_nop 1
	v_mov_b32_e32 v2, vcc_lo
	v_mov_b32_e32 v9, vcc_hi
	v_cmp_ne_u32_e32 vcc, 0, v165
	v_cndmask_b32_e64 v2, 0, v2, s[22:23]
	v_cndmask_b32_e64 v9, 0, v9, s[22:23]
	v_mov_b32_e32 v11, vcc_hi
	v_mov_b32_e32 v14, vcc_lo
	v_cndmask_b32_e64 v9, v9, v11, s[6:7]
	v_cndmask_b32_e64 v2, v2, v14, s[6:7]
	v_cmp_ne_u32_e32 vcc, 0, v166
	s_nop 1
	v_mov_b32_e32 v11, vcc_lo
	v_mov_b32_e32 v14, vcc_hi
	v_cmp_ne_u32_e32 vcc, 0, v167
	v_cndmask_b32_e64 v2, v2, v11, s[8:9]
	v_cndmask_b32_e64 v9, v9, v14, s[8:9]
	v_mov_b32_e32 v11, vcc_hi
	v_mov_b32_e32 v14, vcc_lo
	v_cmp_ne_u32_e32 vcc, 0, v168
	v_cndmask_b32_e64 v9, v9, v11, s[10:11]
	v_cndmask_b32_e64 v2, v2, v14, s[10:11]
	v_mov_b32_e32 v11, vcc_lo
	v_mov_b32_e32 v12, vcc_hi
	v_cmp_ne_u32_e32 vcc, 0, v169
	v_cndmask_b32_e64 v2, v2, v11, s[12:13]
	v_cndmask_b32_e64 v9, v9, v12, s[12:13]
	v_mov_b32_e32 v11, vcc_hi
	v_mov_b32_e32 v12, vcc_lo
	v_cndmask_b32_e64 v9, v9, v11, s[14:15]
	v_cndmask_b32_e64 v2, v2, v12, s[14:15]
	v_cmp_ne_u32_e32 vcc, 0, v170
	s_nop 1
	v_mov_b32_e32 v10, vcc_lo
	v_mov_b32_e32 v11, vcc_hi
	v_cmp_ne_u32_e32 vcc, 0, v171
	v_cndmask_b32_e64 v2, v2, v10, s[16:17]
	v_cndmask_b32_e64 v8, v9, v11, s[16:17]
	v_mov_b32_e32 v9, vcc_hi
	v_mov_b32_e32 v10, vcc_lo
	v_cndmask_b32_e64 v9, v8, v9, s[18:19]
	v_cndmask_b32_e64 v8, v2, v10, s[18:19]
	s_mov_b64 s[2:3], exec
	s_mov_b64 exec, s[0:1]
	global_store_dwordx2 v[4:5], v[8:9], off
	s_mov_b64 exec, s[2:3]
	v_cmp_ne_u64_e32 vcc, 0, v[8:9]
	s_and_b64 s[20:21], s[0:1], vcc
	s_cmp_lg_u64 s[20:21], 0
	s_cselect_b32 s20, 256, 0
	s_or_b32 s76, s76, s20
	v_cmp_ne_u64_e32 vcc, -1, v[8:9]
	s_and_b64 s[20:21], s[0:1], vcc
	s_cmp_lg_u64 s[20:21], 0
	s_cselect_b32 s20, 256, 0
	s_or_b32 s77, s77, s20
	v_lshl_add_u64 v[4:5], v[4:5], 0, 8
	global_load_dword v220, v96, s[60:61] offset:3840 nt
	global_load_dword v221, v96, s[62:63] offset:3840 nt
	global_load_dword v222, v96, s[64:65] offset:3840 nt
	global_load_dword v223, v96, s[66:67] offset:3840 nt
	global_load_dword v224, v96, s[68:69] offset:3840 nt
	global_load_dword v225, v96, s[70:71] offset:3840 nt
	global_load_dword v226, v96, s[72:73] offset:3840 nt
	global_load_dword v227, v96, s[74:75] offset:3840 nt
	s_waitcnt vmcnt(54)
	v_cmp_ne_u32_e32 vcc, 0, v172
	s_nop 1
	v_mov_b32_e32 v2, vcc_lo
	v_mov_b32_e32 v9, vcc_hi
	v_cmp_ne_u32_e32 vcc, 0, v173
	v_cndmask_b32_e64 v2, 0, v2, s[22:23]
	v_cndmask_b32_e64 v9, 0, v9, s[22:23]
	v_mov_b32_e32 v11, vcc_hi
	v_mov_b32_e32 v14, vcc_lo
	v_cndmask_b32_e64 v9, v9, v11, s[6:7]
	v_cndmask_b32_e64 v2, v2, v14, s[6:7]
	v_cmp_ne_u32_e32 vcc, 0, v174
	s_nop 1
	v_mov_b32_e32 v11, vcc_lo
	v_mov_b32_e32 v14, vcc_hi
	v_cmp_ne_u32_e32 vcc, 0, v175
	v_cndmask_b32_e64 v2, v2, v11, s[8:9]
	v_cndmask_b32_e64 v9, v9, v14, s[8:9]
	v_mov_b32_e32 v11, vcc_hi
	v_mov_b32_e32 v14, vcc_lo
	v_cmp_ne_u32_e32 vcc, 0, v176
	v_cndmask_b32_e64 v9, v9, v11, s[10:11]
	v_cndmask_b32_e64 v2, v2, v14, s[10:11]
	v_mov_b32_e32 v11, vcc_lo
	v_mov_b32_e32 v12, vcc_hi
	v_cmp_ne_u32_e32 vcc, 0, v177
	v_cndmask_b32_e64 v2, v2, v11, s[12:13]
	v_cndmask_b32_e64 v9, v9, v12, s[12:13]
	v_mov_b32_e32 v11, vcc_hi
	v_mov_b32_e32 v12, vcc_lo
	v_cndmask_b32_e64 v9, v9, v11, s[14:15]
	v_cndmask_b32_e64 v2, v2, v12, s[14:15]
	v_cmp_ne_u32_e32 vcc, 0, v178
	s_nop 1
	v_mov_b32_e32 v10, vcc_lo
	v_mov_b32_e32 v11, vcc_hi
	v_cmp_ne_u32_e32 vcc, 0, v179
	v_cndmask_b32_e64 v2, v2, v10, s[16:17]
	v_cndmask_b32_e64 v8, v9, v11, s[16:17]
	v_mov_b32_e32 v9, vcc_hi
	v_mov_b32_e32 v10, vcc_lo
	v_cndmask_b32_e64 v9, v8, v9, s[18:19]
	v_cndmask_b32_e64 v8, v2, v10, s[18:19]
	s_mov_b64 s[2:3], exec
	s_mov_b64 exec, s[0:1]
	global_store_dwordx2 v[4:5], v[8:9], off
	s_mov_b64 exec, s[2:3]
	v_cmp_ne_u64_e32 vcc, 0, v[8:9]
	s_and_b64 s[20:21], s[0:1], vcc
	s_cmp_lg_u64 s[20:21], 0
	s_cselect_b32 s20, 512, 0
	s_or_b32 s76, s76, s20
	v_cmp_ne_u64_e32 vcc, -1, v[8:9]
	s_and_b64 s[20:21], s[0:1], vcc
	s_cmp_lg_u64 s[20:21], 0
	s_cselect_b32 s20, 512, 0
	s_or_b32 s77, s77, s20
	v_lshl_add_u64 v[4:5], v[4:5], 0, 8
	s_waitcnt vmcnt(46)
	v_cmp_ne_u32_e32 vcc, 0, v180
	s_nop 1
	v_mov_b32_e32 v2, vcc_lo
	v_mov_b32_e32 v9, vcc_hi
	v_cmp_ne_u32_e32 vcc, 0, v181
	v_cndmask_b32_e64 v2, 0, v2, s[22:23]
	v_cndmask_b32_e64 v9, 0, v9, s[22:23]
	v_mov_b32_e32 v11, vcc_hi
	v_mov_b32_e32 v14, vcc_lo
	v_cndmask_b32_e64 v9, v9, v11, s[6:7]
	v_cndmask_b32_e64 v2, v2, v14, s[6:7]
	v_cmp_ne_u32_e32 vcc, 0, v182
	s_nop 1
	v_mov_b32_e32 v11, vcc_lo
	v_mov_b32_e32 v14, vcc_hi
	v_cmp_ne_u32_e32 vcc, 0, v183
	v_cndmask_b32_e64 v2, v2, v11, s[8:9]
	v_cndmask_b32_e64 v9, v9, v14, s[8:9]
	v_mov_b32_e32 v11, vcc_hi
	v_mov_b32_e32 v14, vcc_lo
	v_cmp_ne_u32_e32 vcc, 0, v184
	v_cndmask_b32_e64 v9, v9, v11, s[10:11]
	v_cndmask_b32_e64 v2, v2, v14, s[10:11]
	v_mov_b32_e32 v11, vcc_lo
	v_mov_b32_e32 v12, vcc_hi
	v_cmp_ne_u32_e32 vcc, 0, v185
	v_cndmask_b32_e64 v2, v2, v11, s[12:13]
	v_cndmask_b32_e64 v9, v9, v12, s[12:13]
	v_mov_b32_e32 v11, vcc_hi
	v_mov_b32_e32 v12, vcc_lo
	v_cndmask_b32_e64 v9, v9, v11, s[14:15]
	v_cndmask_b32_e64 v2, v2, v12, s[14:15]
	v_cmp_ne_u32_e32 vcc, 0, v186
	s_nop 1
	v_mov_b32_e32 v10, vcc_lo
	v_mov_b32_e32 v11, vcc_hi
	v_cmp_ne_u32_e32 vcc, 0, v187
	v_cndmask_b32_e64 v2, v2, v10, s[16:17]
	v_cndmask_b32_e64 v8, v9, v11, s[16:17]
	v_mov_b32_e32 v9, vcc_hi
	v_mov_b32_e32 v10, vcc_lo
	v_cndmask_b32_e64 v9, v8, v9, s[18:19]
	v_cndmask_b32_e64 v8, v2, v10, s[18:19]
	s_mov_b64 s[2:3], exec
	s_mov_b64 exec, s[0:1]
	global_store_dwordx2 v[4:5], v[8:9], off
	s_mov_b64 exec, s[2:3]
	v_cmp_ne_u64_e32 vcc, 0, v[8:9]
	s_and_b64 s[20:21], s[0:1], vcc
	s_cmp_lg_u64 s[20:21], 0
	s_cselect_b32 s20, 1024, 0
	s_or_b32 s76, s76, s20
	v_cmp_ne_u64_e32 vcc, -1, v[8:9]
	s_and_b64 s[20:21], s[0:1], vcc
	s_cmp_lg_u64 s[20:21], 0
	s_cselect_b32 s20, 1024, 0
	s_or_b32 s77, s77, s20
	v_lshl_add_u64 v[4:5], v[4:5], 0, 8
	s_waitcnt vmcnt(38)
	v_cmp_ne_u32_e32 vcc, 0, v188
	s_nop 1
	v_mov_b32_e32 v2, vcc_lo
	v_mov_b32_e32 v9, vcc_hi
	v_cmp_ne_u32_e32 vcc, 0, v189
	v_cndmask_b32_e64 v2, 0, v2, s[22:23]
	v_cndmask_b32_e64 v9, 0, v9, s[22:23]
	v_mov_b32_e32 v11, vcc_hi
	v_mov_b32_e32 v14, vcc_lo
	v_cndmask_b32_e64 v9, v9, v11, s[6:7]
	v_cndmask_b32_e64 v2, v2, v14, s[6:7]
	v_cmp_ne_u32_e32 vcc, 0, v190
	s_nop 1
	v_mov_b32_e32 v11, vcc_lo
	v_mov_b32_e32 v14, vcc_hi
	v_cmp_ne_u32_e32 vcc, 0, v191
	v_cndmask_b32_e64 v2, v2, v11, s[8:9]
	v_cndmask_b32_e64 v9, v9, v14, s[8:9]
	v_mov_b32_e32 v11, vcc_hi
	v_mov_b32_e32 v14, vcc_lo
	v_cmp_ne_u32_e32 vcc, 0, v192
	v_cndmask_b32_e64 v9, v9, v11, s[10:11]
	v_cndmask_b32_e64 v2, v2, v14, s[10:11]
	v_mov_b32_e32 v11, vcc_lo
	v_mov_b32_e32 v12, vcc_hi
	v_cmp_ne_u32_e32 vcc, 0, v193
	v_cndmask_b32_e64 v2, v2, v11, s[12:13]
	v_cndmask_b32_e64 v9, v9, v12, s[12:13]
	v_mov_b32_e32 v11, vcc_hi
	v_mov_b32_e32 v12, vcc_lo
	v_cndmask_b32_e64 v9, v9, v11, s[14:15]
	v_cndmask_b32_e64 v2, v2, v12, s[14:15]
	v_cmp_ne_u32_e32 vcc, 0, v194
	s_nop 1
	v_mov_b32_e32 v10, vcc_lo
	v_mov_b32_e32 v11, vcc_hi
	v_cmp_ne_u32_e32 vcc, 0, v195
	v_cndmask_b32_e64 v2, v2, v10, s[16:17]
	v_cndmask_b32_e64 v8, v9, v11, s[16:17]
	v_mov_b32_e32 v9, vcc_hi
	v_mov_b32_e32 v10, vcc_lo
	v_cndmask_b32_e64 v9, v8, v9, s[18:19]
	v_cndmask_b32_e64 v8, v2, v10, s[18:19]
	s_mov_b64 s[2:3], exec
	s_mov_b64 exec, s[0:1]
	global_store_dwordx2 v[4:5], v[8:9], off
	s_mov_b64 exec, s[2:3]
	v_cmp_ne_u64_e32 vcc, 0, v[8:9]
	s_and_b64 s[20:21], s[0:1], vcc
	s_cmp_lg_u64 s[20:21], 0
	s_cselect_b32 s20, 2048, 0
	s_or_b32 s76, s76, s20
	v_cmp_ne_u64_e32 vcc, -1, v[8:9]
	s_and_b64 s[20:21], s[0:1], vcc
	s_cmp_lg_u64 s[20:21], 0
	s_cselect_b32 s20, 2048, 0
	s_or_b32 s77, s77, s20
	v_lshl_add_u64 v[4:5], v[4:5], 0, 8
	s_waitcnt vmcnt(30)
	v_cmp_ne_u32_e32 vcc, 0, v196
	s_nop 1
	v_mov_b32_e32 v2, vcc_lo
	v_mov_b32_e32 v9, vcc_hi
	v_cmp_ne_u32_e32 vcc, 0, v197
	v_cndmask_b32_e64 v2, 0, v2, s[22:23]
	v_cndmask_b32_e64 v9, 0, v9, s[22:23]
	v_mov_b32_e32 v11, vcc_hi
	v_mov_b32_e32 v14, vcc_lo
	v_cndmask_b32_e64 v9, v9, v11, s[6:7]
	v_cndmask_b32_e64 v2, v2, v14, s[6:7]
	v_cmp_ne_u32_e32 vcc, 0, v198
	s_nop 1
	v_mov_b32_e32 v11, vcc_lo
	v_mov_b32_e32 v14, vcc_hi
	v_cmp_ne_u32_e32 vcc, 0, v199
	v_cndmask_b32_e64 v2, v2, v11, s[8:9]
	v_cndmask_b32_e64 v9, v9, v14, s[8:9]
	v_mov_b32_e32 v11, vcc_hi
	v_mov_b32_e32 v14, vcc_lo
	v_cmp_ne_u32_e32 vcc, 0, v200
	v_cndmask_b32_e64 v9, v9, v11, s[10:11]
	v_cndmask_b32_e64 v2, v2, v14, s[10:11]
	v_mov_b32_e32 v11, vcc_lo
	v_mov_b32_e32 v12, vcc_hi
	v_cmp_ne_u32_e32 vcc, 0, v201
	v_cndmask_b32_e64 v2, v2, v11, s[12:13]
	v_cndmask_b32_e64 v9, v9, v12, s[12:13]
	v_mov_b32_e32 v11, vcc_hi
	v_mov_b32_e32 v12, vcc_lo
	v_cndmask_b32_e64 v9, v9, v11, s[14:15]
	v_cndmask_b32_e64 v2, v2, v12, s[14:15]
	v_cmp_ne_u32_e32 vcc, 0, v202
	s_nop 1
	v_mov_b32_e32 v10, vcc_lo
	v_mov_b32_e32 v11, vcc_hi
	v_cmp_ne_u32_e32 vcc, 0, v203
	v_cndmask_b32_e64 v2, v2, v10, s[16:17]
	v_cndmask_b32_e64 v8, v9, v11, s[16:17]
	v_mov_b32_e32 v9, vcc_hi
	v_mov_b32_e32 v10, vcc_lo
	v_cndmask_b32_e64 v9, v8, v9, s[18:19]
	v_cndmask_b32_e64 v8, v2, v10, s[18:19]
	s_mov_b64 s[2:3], exec
	s_mov_b64 exec, s[0:1]
	global_store_dwordx2 v[4:5], v[8:9], off
	s_mov_b64 exec, s[2:3]
	v_cmp_ne_u64_e32 vcc, 0, v[8:9]
	s_and_b64 s[20:21], s[0:1], vcc
	s_cmp_lg_u64 s[20:21], 0
	s_cselect_b32 s20, 4096, 0
	s_or_b32 s76, s76, s20
	v_cmp_ne_u64_e32 vcc, -1, v[8:9]
	s_and_b64 s[20:21], s[0:1], vcc
	s_cmp_lg_u64 s[20:21], 0
	s_cselect_b32 s20, 4096, 0
	s_or_b32 s77, s77, s20
	v_lshl_add_u64 v[4:5], v[4:5], 0, 8
	s_waitcnt vmcnt(22)
	v_cmp_ne_u32_e32 vcc, 0, v204
	s_nop 1
	v_mov_b32_e32 v2, vcc_lo
	v_mov_b32_e32 v9, vcc_hi
	v_cmp_ne_u32_e32 vcc, 0, v205
	v_cndmask_b32_e64 v2, 0, v2, s[22:23]
	v_cndmask_b32_e64 v9, 0, v9, s[22:23]
	v_mov_b32_e32 v11, vcc_hi
	v_mov_b32_e32 v14, vcc_lo
	v_cndmask_b32_e64 v9, v9, v11, s[6:7]
	v_cndmask_b32_e64 v2, v2, v14, s[6:7]
	v_cmp_ne_u32_e32 vcc, 0, v206
	s_nop 1
	v_mov_b32_e32 v11, vcc_lo
	v_mov_b32_e32 v14, vcc_hi
	v_cmp_ne_u32_e32 vcc, 0, v207
	v_cndmask_b32_e64 v2, v2, v11, s[8:9]
	v_cndmask_b32_e64 v9, v9, v14, s[8:9]
	v_mov_b32_e32 v11, vcc_hi
	v_mov_b32_e32 v14, vcc_lo
	v_cmp_ne_u32_e32 vcc, 0, v208
	v_cndmask_b32_e64 v9, v9, v11, s[10:11]
	v_cndmask_b32_e64 v2, v2, v14, s[10:11]
	v_mov_b32_e32 v11, vcc_lo
	v_mov_b32_e32 v12, vcc_hi
	v_cmp_ne_u32_e32 vcc, 0, v209
	v_cndmask_b32_e64 v2, v2, v11, s[12:13]
	v_cndmask_b32_e64 v9, v9, v12, s[12:13]
	v_mov_b32_e32 v11, vcc_hi
	v_mov_b32_e32 v12, vcc_lo
	v_cndmask_b32_e64 v9, v9, v11, s[14:15]
	v_cndmask_b32_e64 v2, v2, v12, s[14:15]
	v_cmp_ne_u32_e32 vcc, 0, v210
	s_nop 1
	v_mov_b32_e32 v10, vcc_lo
	v_mov_b32_e32 v11, vcc_hi
	v_cmp_ne_u32_e32 vcc, 0, v211
	v_cndmask_b32_e64 v2, v2, v10, s[16:17]
	v_cndmask_b32_e64 v8, v9, v11, s[16:17]
	v_mov_b32_e32 v9, vcc_hi
	v_mov_b32_e32 v10, vcc_lo
	v_cndmask_b32_e64 v9, v8, v9, s[18:19]
	v_cndmask_b32_e64 v8, v2, v10, s[18:19]
	s_mov_b64 s[2:3], exec
	s_mov_b64 exec, s[0:1]
	global_store_dwordx2 v[4:5], v[8:9], off
	s_mov_b64 exec, s[2:3]
	v_cmp_ne_u64_e32 vcc, 0, v[8:9]
	s_and_b64 s[20:21], s[0:1], vcc
	s_cmp_lg_u64 s[20:21], 0
	s_cselect_b32 s20, 8192, 0
	s_or_b32 s76, s76, s20
	v_cmp_ne_u64_e32 vcc, -1, v[8:9]
	s_and_b64 s[20:21], s[0:1], vcc
	s_cmp_lg_u64 s[20:21], 0
	s_cselect_b32 s20, 8192, 0
	s_or_b32 s77, s77, s20
	v_lshl_add_u64 v[4:5], v[4:5], 0, 8
	s_waitcnt vmcnt(14)
	v_cmp_ne_u32_e32 vcc, 0, v212
	s_nop 1
	v_mov_b32_e32 v2, vcc_lo
	v_mov_b32_e32 v9, vcc_hi
	v_cmp_ne_u32_e32 vcc, 0, v213
	v_cndmask_b32_e64 v2, 0, v2, s[22:23]
	v_cndmask_b32_e64 v9, 0, v9, s[22:23]
	v_mov_b32_e32 v11, vcc_hi
	v_mov_b32_e32 v14, vcc_lo
	v_cndmask_b32_e64 v9, v9, v11, s[6:7]
	v_cndmask_b32_e64 v2, v2, v14, s[6:7]
	v_cmp_ne_u32_e32 vcc, 0, v214
	s_nop 1
	v_mov_b32_e32 v11, vcc_lo
	v_mov_b32_e32 v14, vcc_hi
	v_cmp_ne_u32_e32 vcc, 0, v215
	v_cndmask_b32_e64 v2, v2, v11, s[8:9]
	v_cndmask_b32_e64 v9, v9, v14, s[8:9]
	v_mov_b32_e32 v11, vcc_hi
	v_mov_b32_e32 v14, vcc_lo
	v_cmp_ne_u32_e32 vcc, 0, v216
	v_cndmask_b32_e64 v9, v9, v11, s[10:11]
	v_cndmask_b32_e64 v2, v2, v14, s[10:11]
	v_mov_b32_e32 v11, vcc_lo
	v_mov_b32_e32 v12, vcc_hi
	v_cmp_ne_u32_e32 vcc, 0, v217
	v_cndmask_b32_e64 v2, v2, v11, s[12:13]
	v_cndmask_b32_e64 v9, v9, v12, s[12:13]
	v_mov_b32_e32 v11, vcc_hi
	v_mov_b32_e32 v12, vcc_lo
	v_cndmask_b32_e64 v9, v9, v11, s[14:15]
	v_cndmask_b32_e64 v2, v2, v12, s[14:15]
	v_cmp_ne_u32_e32 vcc, 0, v218
	s_nop 1
	v_mov_b32_e32 v10, vcc_lo
	v_mov_b32_e32 v11, vcc_hi
	v_cmp_ne_u32_e32 vcc, 0, v219
	v_cndmask_b32_e64 v2, v2, v10, s[16:17]
	v_cndmask_b32_e64 v8, v9, v11, s[16:17]
	v_mov_b32_e32 v9, vcc_hi
	v_mov_b32_e32 v10, vcc_lo
	v_cndmask_b32_e64 v9, v8, v9, s[18:19]
	v_cndmask_b32_e64 v8, v2, v10, s[18:19]
	s_mov_b64 s[2:3], exec
	s_mov_b64 exec, s[0:1]
	global_store_dwordx2 v[4:5], v[8:9], off
	s_mov_b64 exec, s[2:3]
	v_cmp_ne_u64_e32 vcc, 0, v[8:9]
	s_and_b64 s[20:21], s[0:1], vcc
	s_cmp_lg_u64 s[20:21], 0
	s_cselect_b32 s20, 16384, 0
	s_or_b32 s76, s76, s20
	v_cmp_ne_u64_e32 vcc, -1, v[8:9]
	s_and_b64 s[20:21], s[0:1], vcc
	s_cmp_lg_u64 s[20:21], 0
	s_cselect_b32 s20, 16384, 0
	s_or_b32 s77, s77, s20
	v_lshl_add_u64 v[4:5], v[4:5], 0, 8
	s_waitcnt vmcnt(6)
	v_cmp_ne_u32_e32 vcc, 0, v220
	s_nop 1
	v_mov_b32_e32 v2, vcc_lo
	v_mov_b32_e32 v9, vcc_hi
	v_cmp_ne_u32_e32 vcc, 0, v221
	v_cndmask_b32_e64 v2, 0, v2, s[22:23]
	v_cndmask_b32_e64 v9, 0, v9, s[22:23]
	v_mov_b32_e32 v11, vcc_hi
	v_mov_b32_e32 v14, vcc_lo
	v_cndmask_b32_e64 v9, v9, v11, s[6:7]
	v_cndmask_b32_e64 v2, v2, v14, s[6:7]
	v_cmp_ne_u32_e32 vcc, 0, v222
	s_nop 1
	v_mov_b32_e32 v11, vcc_lo
	v_mov_b32_e32 v14, vcc_hi
	v_cmp_ne_u32_e32 vcc, 0, v223
	v_cndmask_b32_e64 v2, v2, v11, s[8:9]
	v_cndmask_b32_e64 v9, v9, v14, s[8:9]
	v_mov_b32_e32 v11, vcc_hi
	v_mov_b32_e32 v14, vcc_lo
	v_cmp_ne_u32_e32 vcc, 0, v224
	v_cndmask_b32_e64 v9, v9, v11, s[10:11]
	v_cndmask_b32_e64 v2, v2, v14, s[10:11]
	v_mov_b32_e32 v11, vcc_lo
	v_mov_b32_e32 v12, vcc_hi
	v_cmp_ne_u32_e32 vcc, 0, v225
	v_cndmask_b32_e64 v2, v2, v11, s[12:13]
	v_cndmask_b32_e64 v9, v9, v12, s[12:13]
	v_mov_b32_e32 v11, vcc_hi
	v_mov_b32_e32 v12, vcc_lo
	v_cndmask_b32_e64 v9, v9, v11, s[14:15]
	v_cndmask_b32_e64 v2, v2, v12, s[14:15]
	v_cmp_ne_u32_e32 vcc, 0, v226
	s_nop 1
	v_mov_b32_e32 v10, vcc_lo
	v_mov_b32_e32 v11, vcc_hi
	v_cmp_ne_u32_e32 vcc, 0, v227
	v_cndmask_b32_e64 v2, v2, v10, s[16:17]
	v_cndmask_b32_e64 v8, v9, v11, s[16:17]
	v_mov_b32_e32 v9, vcc_hi
	v_mov_b32_e32 v10, vcc_lo
	v_cndmask_b32_e64 v9, v8, v9, s[18:19]
	v_cndmask_b32_e64 v8, v2, v10, s[18:19]
	s_mov_b64 s[2:3], exec
	s_mov_b64 exec, s[0:1]
	global_store_dwordx2 v[4:5], v[8:9], off
	s_mov_b64 exec, s[2:3]
	v_cmp_ne_u64_e32 vcc, 0, v[8:9]
	s_and_b64 s[20:21], s[0:1], vcc
	s_cmp_lg_u64 s[20:21], 0
	s_cselect_b32 s20, 32768, 0
	s_or_b32 s76, s76, s20
	v_cmp_ne_u64_e32 vcc, -1, v[8:9]
	s_and_b64 s[20:21], s[0:1], vcc
	s_cmp_lg_u64 s[20:21], 0
	s_cselect_b32 s20, 32768, 0
	s_or_b32 s77, s77, s20
	v_lshl_add_u64 v[4:5], v[4:5], 0, 8
	v_mov_b32_e32 v2, s76
	v_mov_b32_e32 v8, s77
	s_mov_b64 s[2:3], exec
	s_mov_b64 exec, s[22:23]
	ds_write2_b32 v1, v2, v8 offset1:8
	s_mov_b64 exec, s[2:3]
	s_waitcnt lgkmcnt(0)
	s_barrier
	ds_read_b128 v[8:11], v3
	ds_read_b128 v[12:15], v3 offset:16
	ds_read_b128 v[16:19], v3 offset:32
	ds_read_b128 v[20:23], v3 offset:48
	s_waitcnt lgkmcnt(0)
	v_or_b32_e32 v8, v8, v9
	v_or3_b32 v8, v8, v10, v11
	v_or3_b32 v8, v8, v12, v13
	v_or3_b32 v8, v8, v14, v15
	v_or_b32_e32 v16, v16, v17
	v_or3_b32 v16, v16, v18, v19
	v_or3_b32 v16, v16, v20, v21
	v_or3_b32 v16, v16, v22, v23
	v_and_b32_e32 v2, 15, v0
	v_lshrrev_b32_e32 v8, v2, v8
	v_and_b32_e32 v8, 1, v8
	v_lshrrev_b32_e32 v16, v2, v16
	v_and_b32_e32 v16, 1, v16
	v_lshl_or_b32 v8, v16, 1, v8
	v_lshlrev_b32_e32 v2, 2, v2
	v_cmp_gt_u32_e32 vcc, 16, v0
	s_and_saveexec_b64 s[2:3], vcc
	global_store_dword v2, v8, s[26:27]
	s_mov_b64 exec, s[2:3]
	v_mov_b32_e32 v230, v0
	s_mov_b32 s79, 0

.LBB1_40:
	v_add_u32_e32 v2, s0, v18
	v_and_b32_e32 v20, 32, v19
	v_ashrrev_i32_e32 v21, 8, v19
	v_and_b32_e32 v22, 0x7c0, v16
	v_add_u32_e32 v23, s0, v14
	v_lshrrev_b32_e32 v34, 7, v2
	v_bitop3_b32 v20, v2, v20, 48 bitop3:0x6c
	v_and_b32_e32 v24, 32, v15
	v_ashrrev_i32_e32 v25, 8, v15
	v_lshrrev_b32_e32 v35, 5, v2
	v_lshrrev_b32_e32 v36, 9, v2
	v_bfe_u32 v37, v2, 6, 2
	v_and_b32_e32 v21, 0xffffff80, v21
	v_lshlrev_b32_e32 v2, 2, v22
	v_lshrrev_b32_e32 v22, 7, v23
	v_lshrrev_b32_e32 v20, 1, v20
	v_and_b32_e32 v34, 0x60, v34
	v_add_u32_e32 v26, s0, v10
	v_lshrrev_b32_e32 v38, 5, v23
	v_bitop3_b32 v24, v23, v24, 48 bitop3:0x6c
	v_lshrrev_b32_e32 v39, 9, v23
	v_bfe_u32 v23, v23, 6, 2
	v_and_b32_e32 v25, 0xffffff80, v25
	v_and_b32_e32 v47, 24, v35
	v_and_b32_e32 v36, 4, v36
	v_and_b32_e32 v22, 0x60, v22
	v_and_or_b32 v35, v35, 32, v20
	v_or3_b32 v20, v37, v21, v34
	v_and_b32_e32 v27, 32, v11
	v_ashrrev_i32_e32 v28, 8, v11
	v_lshrrev_b32_e32 v41, 7, v26
	v_and_b32_e32 v48, 24, v38
	v_and_b32_e32 v39, 4, v39
	v_or3_b32 v21, v23, v25, v22
	v_or3_b32 v20, v20, v36, v47
	v_add_u32_e32 v29, s0, v6
	v_lshrrev_b32_e32 v42, 5, v26
	v_bitop3_b32 v27, v26, v27, 48 bitop3:0x6c
	v_lshrrev_b32_e32 v43, 9, v26
	v_bfe_u32 v26, v26, 6, 2
	v_and_b32_e32 v28, 0xffffff80, v28
	v_and_b32_e32 v41, 0x60, v41
	v_or3_b32 v22, v21, v39, v48
	v_ashrrev_i32_e32 v21, 31, v20
	v_and_b32_e32 v30, 32, v7
	v_ashrrev_i32_e32 v31, 8, v7
	v_lshrrev_b32_e32 v44, 7, v29
	v_lshrrev_b32_e32 v24, 1, v24
	v_and_b32_e32 v49, 24, v42
	v_and_b32_e32 v43, 4, v43
	v_or3_b32 v23, v26, v28, v41
	v_lshlrev_b64 v[20:21], 13, v[20:21]
	v_lshrrev_b32_e32 v45, 5, v29
	v_bitop3_b32 v30, v29, v30, 48 bitop3:0x6c
	v_lshrrev_b32_e32 v46, 9, v29
	v_bfe_u32 v29, v29, 6, 2
	v_and_b32_e32 v31, 0xffffff80, v31
	v_and_b32_e32 v44, 0x60, v44
	v_and_or_b32 v34, v38, 32, v24
	v_or3_b32 v24, v23, v43, v49
	v_ashrrev_i32_e32 v23, 31, v22
	v_lshl_add_u64 v[20:21], s[38:39], 0, v[20:21]
	v_and_b32_e32 v32, 0x7c0, v12
	v_lshrrev_b32_e32 v30, 1, v30
	v_and_b32_e32 v50, 24, v45
	v_and_b32_e32 v46, 4, v46
	v_or3_b32 v25, v29, v31, v44
	v_lshlrev_b64 v[22:23], 13, v[22:23]
	v_lshl_add_u64 v[20:21], v[20:21], 0, v[2:3]
	v_lshlrev_b32_e32 v2, 2, v35
	v_and_or_b32 v51, v45, 32, v30
	v_or3_b32 v26, v25, v46, v50
	v_ashrrev_i32_e32 v25, 31, v24
	v_lshl_add_u64 v[28:29], s[38:39], 0, v[22:23]
	v_lshl_add_u64 v[30:31], v[20:21], 0, v[2:3]
	v_lshlrev_b32_e32 v2, 2, v32
	v_and_b32_e32 v33, 0x7c0, v8
	v_lshrrev_b32_e32 v27, 1, v27
	v_lshlrev_b64 v[24:25], 13, v[24:25]
	v_lshl_add_u64 v[28:29], v[28:29], 0, v[2:3]
	v_lshlrev_b32_e32 v2, 2, v34
	v_and_or_b32 v42, v42, 32, v27
	v_ashrrev_i32_e32 v27, 31, v26
	v_lshl_add_u64 v[36:37], s[38:39], 0, v[24:25]
	v_lshl_add_u64 v[38:39], v[28:29], 0, v[2:3]
	v_lshlrev_b32_e32 v2, 2, v33
	v_and_b32_e32 v40, 0x7c0, v0
	v_lshlrev_b64 v[26:27], 13, v[26:27]
	v_lshl_add_u64 v[36:37], v[36:37], 0, v[2:3]
	v_lshlrev_b32_e32 v2, 2, v42
	v_lshl_add_u64 v[44:45], s[38:39], 0, v[26:27]
	global_load_dwordx4 v[20:23], v[30:31], off nt
	global_load_dwordx4 v[24:27], v[30:31], off offset:16 nt
	v_lshl_add_u64 v[46:47], v[36:37], 0, v[2:3]
	v_lshlrev_b32_e32 v2, 2, v40
	global_load_dwordx4 v[28:31], v[38:39], off offset:16 nt
	global_load_dwordx4 v[32:35], v[38:39], off nt
	v_lshl_add_u64 v[44:45], v[44:45], 0, v[2:3]
	v_lshlrev_b32_e32 v2, 2, v51
	global_load_dwordx4 v[36:39], v[46:47], off nt
	global_load_dwordx4 v[40:43], v[46:47], off offset:16 nt
	v_lshl_add_u64 v[52:53], v[44:45], 0, v[2:3]
	global_load_dwordx4 v[44:47], v[52:53], off nt
	global_load_dwordx4 v[48:51], v[52:53], off offset:16 nt
	v_lshl_add_u64 v[52:53], v[4:5], 0, s[0:1]
	v_add_co_u32_e32 v54, vcc, s4, v52
	s_add_u32 s0, s0, 0x8000
	s_nop 0
	v_addc_co_u32_e32 v55, vcc, 0, v53, vcc
	v_add_co_u32_e32 v56, vcc, s5, v52
	s_addc_u32 s1, s1, 0
	s_nop 0
	v_addc_co_u32_e32 v57, vcc, 0, v53, vcc
	v_add_co_u32_e32 v58, vcc, s6, v52
	v_lshl_add_u64 v[0:1], v[0:1], 0, s[2:3]
	v_add_u32_e32 v7, 0x800, v7
	v_lshl_add_u64 v[8:9], v[8:9], 0, s[2:3]
	v_add_u32_e32 v11, 0x800, v11
	v_lshl_add_u64 v[12:13], v[12:13], 0, s[2:3]
	v_add_u32_e32 v15, 0x800, v15
	v_lshl_add_u64 v[16:17], v[16:17], 0, s[2:3]
	v_add_u32_e32 v19, 0x800, v19
	v_addc_co_u32_e32 v59, vcc, 0, v53, vcc
	v_add_u32_e32 v2, s0, v18
	v_and_b32_e32 v60, 32, v19
	v_ashrrev_i32_e32 v61, 8, v19
	v_and_b32_e32 v62, 0x7c0, v16
	v_add_u32_e32 v63, s0, v14
	v_lshrrev_b32_e32 v74, 7, v2
	v_bitop3_b32 v60, v2, v60, 48 bitop3:0x6c
	v_and_b32_e32 v64, 32, v15
	v_ashrrev_i32_e32 v65, 8, v15
	v_lshrrev_b32_e32 v75, 5, v2
	v_lshrrev_b32_e32 v76, 9, v2
	v_bfe_u32 v77, v2, 6, 2
	v_and_b32_e32 v61, 0xffffff80, v61
	v_lshlrev_b32_e32 v2, 2, v62
	v_lshrrev_b32_e32 v62, 7, v63
	v_lshrrev_b32_e32 v60, 1, v60
	v_and_b32_e32 v74, 0x60, v74
	v_add_u32_e32 v66, s0, v10
	v_lshrrev_b32_e32 v78, 5, v63
	v_bitop3_b32 v64, v63, v64, 48 bitop3:0x6c
	v_lshrrev_b32_e32 v79, 9, v63
	v_bfe_u32 v63, v63, 6, 2
	v_and_b32_e32 v65, 0xffffff80, v65
	v_and_b32_e32 v87, 24, v75
	v_and_b32_e32 v76, 4, v76
	v_and_b32_e32 v62, 0x60, v62
	v_and_or_b32 v75, v75, 32, v60
	v_or3_b32 v60, v77, v61, v74
	v_and_b32_e32 v67, 32, v11
	v_ashrrev_i32_e32 v68, 8, v11
	v_lshrrev_b32_e32 v81, 7, v66
	v_and_b32_e32 v88, 24, v78
	v_and_b32_e32 v79, 4, v79
	v_or3_b32 v61, v63, v65, v62
	v_or3_b32 v60, v60, v76, v87
	v_add_u32_e32 v69, s0, v6
	v_lshrrev_b32_e32 v82, 5, v66
	v_bitop3_b32 v67, v66, v67, 48 bitop3:0x6c
	v_lshrrev_b32_e32 v83, 9, v66
	v_bfe_u32 v66, v66, 6, 2
	v_and_b32_e32 v68, 0xffffff80, v68
	v_and_b32_e32 v81, 0x60, v81
	v_or3_b32 v62, v61, v79, v88
	v_ashrrev_i32_e32 v61, 31, v60
	v_and_b32_e32 v70, 32, v7
	v_ashrrev_i32_e32 v71, 8, v7
	v_lshrrev_b32_e32 v84, 7, v69
	v_lshrrev_b32_e32 v64, 1, v64
	v_and_b32_e32 v89, 24, v82
	v_and_b32_e32 v83, 4, v83
	v_or3_b32 v63, v66, v68, v81
	v_lshlrev_b64 v[60:61], 13, v[60:61]
	v_lshrrev_b32_e32 v85, 5, v69
	v_bitop3_b32 v70, v69, v70, 48 bitop3:0x6c
	v_lshrrev_b32_e32 v86, 9, v69
	v_bfe_u32 v69, v69, 6, 2
	v_and_b32_e32 v71, 0xffffff80, v71
	v_and_b32_e32 v84, 0x60, v84
	v_and_or_b32 v74, v78, 32, v64
	v_or3_b32 v64, v63, v83, v89
	v_ashrrev_i32_e32 v63, 31, v62
	v_lshl_add_u64 v[60:61], s[38:39], 0, v[60:61]
	v_and_b32_e32 v72, 0x7c0, v12
	v_lshrrev_b32_e32 v70, 1, v70
	v_and_b32_e32 v90, 24, v85
	v_and_b32_e32 v86, 4, v86
	v_or3_b32 v65, v69, v71, v84
	v_lshlrev_b64 v[62:63], 13, v[62:63]
	v_lshl_add_u64 v[60:61], v[60:61], 0, v[2:3]
	v_lshlrev_b32_e32 v2, 2, v75
	v_and_or_b32 v91, v85, 32, v70
	v_or3_b32 v66, v65, v86, v90
	v_ashrrev_i32_e32 v65, 31, v64
	v_lshl_add_u64 v[68:69], s[38:39], 0, v[62:63]
	v_lshl_add_u64 v[70:71], v[60:61], 0, v[2:3]
	v_lshlrev_b32_e32 v2, 2, v72
	v_and_b32_e32 v73, 0x7c0, v8
	v_lshrrev_b32_e32 v67, 1, v67
	v_lshlrev_b64 v[64:65], 13, v[64:65]
	v_lshl_add_u64 v[68:69], v[68:69], 0, v[2:3]
	v_lshlrev_b32_e32 v2, 2, v74
	v_and_or_b32 v82, v82, 32, v67
	v_ashrrev_i32_e32 v67, 31, v66
	v_lshl_add_u64 v[76:77], s[38:39], 0, v[64:65]
	v_lshl_add_u64 v[78:79], v[68:69], 0, v[2:3]
	v_lshlrev_b32_e32 v2, 2, v73
	v_and_b32_e32 v80, 0x7c0, v0
	v_lshlrev_b64 v[66:67], 13, v[66:67]
	v_lshl_add_u64 v[76:77], v[76:77], 0, v[2:3]
	v_lshlrev_b32_e32 v2, 2, v82
	v_lshl_add_u64 v[84:85], s[38:39], 0, v[66:67]
	global_load_dwordx4 v[60:63], v[70:71], off nt
	global_load_dwordx4 v[64:67], v[70:71], off offset:16 nt
	v_lshl_add_u64 v[86:87], v[76:77], 0, v[2:3]
	v_lshlrev_b32_e32 v2, 2, v80
	global_load_dwordx4 v[68:71], v[78:79], off offset:16 nt
	global_load_dwordx4 v[72:75], v[78:79], off nt
	v_lshl_add_u64 v[84:85], v[84:85], 0, v[2:3]
	v_lshlrev_b32_e32 v2, 2, v91
	global_load_dwordx4 v[76:79], v[86:87], off nt
	global_load_dwordx4 v[80:83], v[86:87], off offset:16 nt
	v_lshl_add_u64 v[92:93], v[84:85], 0, v[2:3]
	global_load_dwordx4 v[84:87], v[92:93], off nt
	global_load_dwordx4 v[88:91], v[92:93], off offset:16 nt
	v_lshl_add_u64 v[92:93], v[4:5], 0, s[0:1]
	v_add_co_u32_e32 v94, vcc, s4, v92
	s_add_u32 s0, s0, 0x8000
	s_nop 0
	v_addc_co_u32_e32 v95, vcc, 0, v93, vcc
	v_add_co_u32_e32 v96, vcc, s5, v92
	s_addc_u32 s1, s1, 0
	s_nop 0
	v_addc_co_u32_e32 v97, vcc, 0, v93, vcc
	v_add_co_u32_e32 v98, vcc, s6, v92
	v_lshl_add_u64 v[0:1], v[0:1], 0, s[2:3]
	v_add_u32_e32 v7, 0x800, v7
	v_lshl_add_u64 v[8:9], v[8:9], 0, s[2:3]
	v_add_u32_e32 v11, 0x800, v11
	v_lshl_add_u64 v[12:13], v[12:13], 0, s[2:3]
	v_add_u32_e32 v15, 0x800, v15
	v_lshl_add_u64 v[16:17], v[16:17], 0, s[2:3]
	v_add_u32_e32 v19, 0x800, v19
	v_addc_co_u32_e32 v99, vcc, 0, v93, vcc
	v_add_u32_e32 v2, s0, v18
	v_and_b32_e32 v100, 32, v19
	v_ashrrev_i32_e32 v101, 8, v19
	v_and_b32_e32 v102, 0x7c0, v16
	v_add_u32_e32 v103, s0, v14
	v_lshrrev_b32_e32 v114, 7, v2
	v_bitop3_b32 v100, v2, v100, 48 bitop3:0x6c
	v_and_b32_e32 v104, 32, v15
	v_ashrrev_i32_e32 v105, 8, v15
	v_lshrrev_b32_e32 v115, 5, v2
	v_lshrrev_b32_e32 v116, 9, v2
	v_bfe_u32 v117, v2, 6, 2
	v_and_b32_e32 v101, 0xffffff80, v101
	v_lshlrev_b32_e32 v2, 2, v102
	v_lshrrev_b32_e32 v102, 7, v103
	v_lshrrev_b32_e32 v100, 1, v100
	v_and_b32_e32 v114, 0x60, v114
	v_add_u32_e32 v106, s0, v10
	v_lshrrev_b32_e32 v118, 5, v103
	v_bitop3_b32 v104, v103, v104, 48 bitop3:0x6c
	v_lshrrev_b32_e32 v119, 9, v103
	v_bfe_u32 v103, v103, 6, 2
	v_and_b32_e32 v105, 0xffffff80, v105
	v_and_b32_e32 v127, 24, v115
	v_and_b32_e32 v116, 4, v116
	v_and_b32_e32 v102, 0x60, v102
	v_and_or_b32 v115, v115, 32, v100
	v_or3_b32 v100, v117, v101, v114
	v_and_b32_e32 v107, 32, v11
	v_ashrrev_i32_e32 v108, 8, v11
	v_lshrrev_b32_e32 v121, 7, v106
	v_and_b32_e32 v128, 24, v118
	v_and_b32_e32 v119, 4, v119
	v_or3_b32 v101, v103, v105, v102
	v_or3_b32 v100, v100, v116, v127
	v_add_u32_e32 v109, s0, v6
	v_lshrrev_b32_e32 v122, 5, v106
	v_bitop3_b32 v107, v106, v107, 48 bitop3:0x6c
	v_lshrrev_b32_e32 v123, 9, v106
	v_bfe_u32 v106, v106, 6, 2
	v_and_b32_e32 v108, 0xffffff80, v108
	v_and_b32_e32 v121, 0x60, v121
	v_or3_b32 v102, v101, v119, v128
	v_ashrrev_i32_e32 v101, 31, v100
	v_and_b32_e32 v110, 32, v7
	v_ashrrev_i32_e32 v111, 8, v7
	v_lshrrev_b32_e32 v124, 7, v109
	v_lshrrev_b32_e32 v104, 1, v104
	v_and_b32_e32 v129, 24, v122
	v_and_b32_e32 v123, 4, v123
	v_or3_b32 v103, v106, v108, v121
	v_lshlrev_b64 v[100:101], 13, v[100:101]
	v_lshrrev_b32_e32 v125, 5, v109
	v_bitop3_b32 v110, v109, v110, 48 bitop3:0x6c
	v_lshrrev_b32_e32 v126, 9, v109
	v_bfe_u32 v109, v109, 6, 2
	v_and_b32_e32 v111, 0xffffff80, v111
	v_and_b32_e32 v124, 0x60, v124
	v_and_or_b32 v114, v118, 32, v104
	v_or3_b32 v104, v103, v123, v129
	v_ashrrev_i32_e32 v103, 31, v102
	v_lshl_add_u64 v[100:101], s[38:39], 0, v[100:101]
	v_and_b32_e32 v112, 0x7c0, v12
	v_lshrrev_b32_e32 v110, 1, v110
	v_and_b32_e32 v130, 24, v125
	v_and_b32_e32 v126, 4, v126
	v_or3_b32 v105, v109, v111, v124
	v_lshlrev_b64 v[102:103], 13, v[102:103]
	v_lshl_add_u64 v[100:101], v[100:101], 0, v[2:3]
	v_lshlrev_b32_e32 v2, 2, v115
	v_and_or_b32 v131, v125, 32, v110
	v_or3_b32 v106, v105, v126, v130
	v_ashrrev_i32_e32 v105, 31, v104
	v_lshl_add_u64 v[108:109], s[38:39], 0, v[102:103]
	v_lshl_add_u64 v[110:111], v[100:101], 0, v[2:3]
	v_lshlrev_b32_e32 v2, 2, v112
	v_and_b32_e32 v113, 0x7c0, v8
	v_lshrrev_b32_e32 v107, 1, v107
	v_lshlrev_b64 v[104:105], 13, v[104:105]
	v_lshl_add_u64 v[108:109], v[108:109], 0, v[2:3]
	v_lshlrev_b32_e32 v2, 2, v114
	v_and_or_b32 v122, v122, 32, v107
	v_ashrrev_i32_e32 v107, 31, v106
	v_lshl_add_u64 v[116:117], s[38:39], 0, v[104:105]
	v_lshl_add_u64 v[118:119], v[108:109], 0, v[2:3]
	v_lshlrev_b32_e32 v2, 2, v113
	v_and_b32_e32 v120, 0x7c0, v0
	v_lshlrev_b64 v[106:107], 13, v[106:107]
	v_lshl_add_u64 v[116:117], v[116:117], 0, v[2:3]
	v_lshlrev_b32_e32 v2, 2, v122
	v_lshl_add_u64 v[124:125], s[38:39], 0, v[106:107]
	global_load_dwordx4 v[100:103], v[110:111], off nt
	global_load_dwordx4 v[104:107], v[110:111], off offset:16 nt
	v_lshl_add_u64 v[126:127], v[116:117], 0, v[2:3]
	v_lshlrev_b32_e32 v2, 2, v120
	global_load_dwordx4 v[108:111], v[118:119], off offset:16 nt
	global_load_dwordx4 v[112:115], v[118:119], off nt
	v_lshl_add_u64 v[124:125], v[124:125], 0, v[2:3]
	v_lshlrev_b32_e32 v2, 2, v131
	global_load_dwordx4 v[116:119], v[126:127], off nt
	global_load_dwordx4 v[120:123], v[126:127], off offset:16 nt
	v_lshl_add_u64 v[132:133], v[124:125], 0, v[2:3]
	global_load_dwordx4 v[124:127], v[132:133], off nt
	global_load_dwordx4 v[128:131], v[132:133], off offset:16 nt
	v_lshl_add_u64 v[132:133], v[4:5], 0, s[0:1]
	v_add_co_u32_e32 v134, vcc, s4, v132
	s_add_u32 s0, s0, 0x8000
	s_nop 0
	v_addc_co_u32_e32 v135, vcc, 0, v133, vcc
	v_add_co_u32_e32 v136, vcc, s5, v132
	s_addc_u32 s1, s1, 0
	s_nop 0
	v_addc_co_u32_e32 v137, vcc, 0, v133, vcc
	v_add_co_u32_e32 v138, vcc, s6, v132
	v_lshl_add_u64 v[0:1], v[0:1], 0, s[2:3]
	v_add_u32_e32 v7, 0x800, v7
	v_lshl_add_u64 v[8:9], v[8:9], 0, s[2:3]
	v_add_u32_e32 v11, 0x800, v11
	v_lshl_add_u64 v[12:13], v[12:13], 0, s[2:3]
	v_add_u32_e32 v15, 0x800, v15
	v_lshl_add_u64 v[16:17], v[16:17], 0, s[2:3]
	v_add_u32_e32 v19, 0x800, v19
	v_addc_co_u32_e32 v139, vcc, 0, v133, vcc
	v_add_u32_e32 v2, s0, v18
	v_and_b32_e32 v140, 32, v19
	v_ashrrev_i32_e32 v141, 8, v19
	v_and_b32_e32 v142, 0x7c0, v16
	v_add_u32_e32 v143, s0, v14
	v_lshrrev_b32_e32 v154, 7, v2
	v_bitop3_b32 v140, v2, v140, 48 bitop3:0x6c
	v_and_b32_e32 v144, 32, v15
	v_ashrrev_i32_e32 v145, 8, v15
	v_lshrrev_b32_e32 v155, 5, v2
	v_lshrrev_b32_e32 v156, 9, v2
	v_bfe_u32 v157, v2, 6, 2
	v_and_b32_e32 v141, 0xffffff80, v141
	v_lshlrev_b32_e32 v2, 2, v142
	v_lshrrev_b32_e32 v142, 7, v143
	v_lshrrev_b32_e32 v140, 1, v140
	v_and_b32_e32 v154, 0x60, v154
	v_add_u32_e32 v146, s0, v10
	v_lshrrev_b32_e32 v158, 5, v143
	v_bitop3_b32 v144, v143, v144, 48 bitop3:0x6c
	v_lshrrev_b32_e32 v159, 9, v143
	v_bfe_u32 v143, v143, 6, 2
	v_and_b32_e32 v145, 0xffffff80, v145
	v_and_b32_e32 v167, 24, v155
	v_and_b32_e32 v156, 4, v156
	v_and_b32_e32 v142, 0x60, v142
	v_and_or_b32 v155, v155, 32, v140
	v_or3_b32 v140, v157, v141, v154
	v_and_b32_e32 v147, 32, v11
	v_ashrrev_i32_e32 v148, 8, v11
	v_lshrrev_b32_e32 v161, 7, v146
	v_and_b32_e32 v168, 24, v158
	v_and_b32_e32 v159, 4, v159
	v_or3_b32 v141, v143, v145, v142
	v_or3_b32 v140, v140, v156, v167
	v_add_u32_e32 v149, s0, v6
	v_lshrrev_b32_e32 v162, 5, v146
	v_bitop3_b32 v147, v146, v147, 48 bitop3:0x6c
	v_lshrrev_b32_e32 v163, 9, v146
	v_bfe_u32 v146, v146, 6, 2
	v_and_b32_e32 v148, 0xffffff80, v148
	v_and_b32_e32 v161, 0x60, v161
	v_or3_b32 v142, v141, v159, v168
	v_ashrrev_i32_e32 v141, 31, v140
	v_and_b32_e32 v150, 32, v7
	v_ashrrev_i32_e32 v151, 8, v7
	v_lshrrev_b32_e32 v164, 7, v149
	v_lshrrev_b32_e32 v144, 1, v144
	v_and_b32_e32 v169, 24, v162
	v_and_b32_e32 v163, 4, v163
	v_or3_b32 v143, v146, v148, v161
	v_lshlrev_b64 v[140:141], 13, v[140:141]
	v_lshrrev_b32_e32 v165, 5, v149
	v_bitop3_b32 v150, v149, v150, 48 bitop3:0x6c
	v_lshrrev_b32_e32 v166, 9, v149
	v_bfe_u32 v149, v149, 6, 2
	v_and_b32_e32 v151, 0xffffff80, v151
	v_and_b32_e32 v164, 0x60, v164
	v_and_or_b32 v154, v158, 32, v144
	v_or3_b32 v144, v143, v163, v169
	v_ashrrev_i32_e32 v143, 31, v142
	v_lshl_add_u64 v[140:141], s[38:39], 0, v[140:141]
	v_and_b32_e32 v152, 0x7c0, v12
	v_lshrrev_b32_e32 v150, 1, v150
	v_and_b32_e32 v170, 24, v165
	v_and_b32_e32 v166, 4, v166
	v_or3_b32 v145, v149, v151, v164
	v_lshlrev_b64 v[142:143], 13, v[142:143]
	v_lshl_add_u64 v[140:141], v[140:141], 0, v[2:3]
	v_lshlrev_b32_e32 v2, 2, v155
	v_and_or_b32 v171, v165, 32, v150
	v_or3_b32 v146, v145, v166, v170
	v_ashrrev_i32_e32 v145, 31, v144
	v_lshl_add_u64 v[148:149], s[38:39], 0, v[142:143]
	v_lshl_add_u64 v[150:151], v[140:141], 0, v[2:3]
	v_lshlrev_b32_e32 v2, 2, v152
	v_and_b32_e32 v153, 0x7c0, v8
	v_lshrrev_b32_e32 v147, 1, v147
	v_lshlrev_b64 v[144:145], 13, v[144:145]
	v_lshl_add_u64 v[148:149], v[148:149], 0, v[2:3]
	v_lshlrev_b32_e32 v2, 2, v154
	v_and_or_b32 v162, v162, 32, v147
	v_ashrrev_i32_e32 v147, 31, v146
	v_lshl_add_u64 v[156:157], s[38:39], 0, v[144:145]
	v_lshl_add_u64 v[158:159], v[148:149], 0, v[2:3]
	v_lshlrev_b32_e32 v2, 2, v153
	v_and_b32_e32 v160, 0x7c0, v0
	v_lshlrev_b64 v[146:147], 13, v[146:147]
	v_lshl_add_u64 v[156:157], v[156:157], 0, v[2:3]
	v_lshlrev_b32_e32 v2, 2, v162
	v_lshl_add_u64 v[164:165], s[38:39], 0, v[146:147]
	global_load_dwordx4 v[140:143], v[150:151], off nt
	global_load_dwordx4 v[144:147], v[150:151], off offset:16 nt
	v_lshl_add_u64 v[166:167], v[156:157], 0, v[2:3]
	v_lshlrev_b32_e32 v2, 2, v160
	global_load_dwordx4 v[148:151], v[158:159], off offset:16 nt
	global_load_dwordx4 v[152:155], v[158:159], off nt
	v_lshl_add_u64 v[164:165], v[164:165], 0, v[2:3]
	v_lshlrev_b32_e32 v2, 2, v171
	global_load_dwordx4 v[156:159], v[166:167], off nt
	global_load_dwordx4 v[160:163], v[166:167], off offset:16 nt
	v_lshl_add_u64 v[172:173], v[164:165], 0, v[2:3]
	global_load_dwordx4 v[164:167], v[172:173], off nt
	global_load_dwordx4 v[168:171], v[172:173], off offset:16 nt
	v_lshl_add_u64 v[172:173], v[4:5], 0, s[0:1]
	v_add_co_u32_e32 v174, vcc, s4, v172
	s_add_u32 s0, s0, 0x8000
	s_nop 0
	v_addc_co_u32_e32 v175, vcc, 0, v173, vcc
	v_add_co_u32_e32 v176, vcc, s5, v172
	s_addc_u32 s1, s1, 0
	s_nop 0
	v_addc_co_u32_e32 v177, vcc, 0, v173, vcc
	v_add_co_u32_e32 v178, vcc, s6, v172
	v_lshl_add_u64 v[0:1], v[0:1], 0, s[2:3]
	v_add_u32_e32 v7, 0x800, v7
	v_lshl_add_u64 v[8:9], v[8:9], 0, s[2:3]
	v_add_u32_e32 v11, 0x800, v11
	v_lshl_add_u64 v[12:13], v[12:13], 0, s[2:3]
	v_add_u32_e32 v15, 0x800, v15
	v_lshl_add_u64 v[16:17], v[16:17], 0, s[2:3]
	v_add_u32_e32 v19, 0x800, v19
	v_addc_co_u32_e32 v179, vcc, 0, v173, vcc
	s_waitcnt vmcnt(31)
	v_cvt_pk_f16_f32 v20, v20, v21
	v_cvt_pk_f16_f32 v21, v22, v23
	s_waitcnt vmcnt(30)
	v_cvt_pk_f16_f32 v22, v24, v25
	v_cvt_pk_f16_f32 v23, v26, v27
	global_store_dwordx4 v[52:53], v[20:23], off sc1
	s_waitcnt vmcnt(29)
	s_nop 0
	v_cvt_pk_f16_f32 v20, v32, v33
	v_cvt_pk_f16_f32 v21, v34, v35
	v_cvt_pk_f16_f32 v22, v28, v29
	v_cvt_pk_f16_f32 v23, v30, v31
	global_store_dwordx4 v[54:55], v[20:23], off sc1
	s_waitcnt vmcnt(29)
	s_nop 0
	v_cvt_pk_f16_f32 v20, v36, v37
	v_cvt_pk_f16_f32 v21, v38, v39
	s_waitcnt vmcnt(28)
	v_cvt_pk_f16_f32 v22, v40, v41
	v_cvt_pk_f16_f32 v23, v42, v43
	global_store_dwordx4 v[56:57], v[20:23], off sc1
	s_waitcnt vmcnt(28)
	s_nop 0
	v_cvt_pk_f16_f32 v20, v44, v45
	v_cvt_pk_f16_f32 v21, v46, v47
	s_waitcnt vmcnt(27)
	v_cvt_pk_f16_f32 v22, v48, v49
	v_cvt_pk_f16_f32 v23, v50, v51
	global_store_dwordx4 v[58:59], v[20:23], off sc1
	s_waitcnt vmcnt(27)
	v_cvt_pk_f16_f32 v60, v60, v61
	v_cvt_pk_f16_f32 v61, v62, v63
	s_waitcnt vmcnt(26)
	v_cvt_pk_f16_f32 v62, v64, v65
	v_cvt_pk_f16_f32 v63, v66, v67
	global_store_dwordx4 v[92:93], v[60:63], off sc1
	s_waitcnt vmcnt(25)
	s_nop 0
	v_cvt_pk_f16_f32 v60, v72, v73
	v_cvt_pk_f16_f32 v61, v74, v75
	v_cvt_pk_f16_f32 v62, v68, v69
	v_cvt_pk_f16_f32 v63, v70, v71
	global_store_dwordx4 v[94:95], v[60:63], off sc1
	s_waitcnt vmcnt(25)
	s_nop 0
	v_cvt_pk_f16_f32 v60, v76, v77
	v_cvt_pk_f16_f32 v61, v78, v79
	s_waitcnt vmcnt(24)
	v_cvt_pk_f16_f32 v62, v80, v81
	v_cvt_pk_f16_f32 v63, v82, v83
	global_store_dwordx4 v[96:97], v[60:63], off sc1
	s_waitcnt vmcnt(24)
	s_nop 0
	v_cvt_pk_f16_f32 v60, v84, v85
	v_cvt_pk_f16_f32 v61, v86, v87
	s_waitcnt vmcnt(23)
	v_cvt_pk_f16_f32 v62, v88, v89
	v_cvt_pk_f16_f32 v63, v90, v91
	global_store_dwordx4 v[98:99], v[60:63], off sc1
	s_waitcnt vmcnt(23)
	v_cvt_pk_f16_f32 v100, v100, v101
	v_cvt_pk_f16_f32 v101, v102, v103
	s_waitcnt vmcnt(22)
	v_cvt_pk_f16_f32 v102, v104, v105
	v_cvt_pk_f16_f32 v103, v106, v107
	global_store_dwordx4 v[132:133], v[100:103], off sc1
	s_waitcnt vmcnt(21)
	s_nop 0
	v_cvt_pk_f16_f32 v100, v112, v113
	v_cvt_pk_f16_f32 v101, v114, v115
	v_cvt_pk_f16_f32 v102, v108, v109
	v_cvt_pk_f16_f32 v103, v110, v111
	global_store_dwordx4 v[134:135], v[100:103], off sc1
	s_waitcnt vmcnt(21)
	s_nop 0
	v_cvt_pk_f16_f32 v100, v116, v117
	v_cvt_pk_f16_f32 v101, v118, v119
	s_waitcnt vmcnt(20)
	v_cvt_pk_f16_f32 v102, v120, v121
	v_cvt_pk_f16_f32 v103, v122, v123
	global_store_dwordx4 v[136:137], v[100:103], off sc1
	s_waitcnt vmcnt(20)
	s_nop 0
	v_cvt_pk_f16_f32 v100, v124, v125
	v_cvt_pk_f16_f32 v101, v126, v127
	s_waitcnt vmcnt(19)
	v_cvt_pk_f16_f32 v102, v128, v129
	v_cvt_pk_f16_f32 v103, v130, v131
	global_store_dwordx4 v[138:139], v[100:103], off sc1
	s_waitcnt vmcnt(19)
	v_cvt_pk_f16_f32 v140, v140, v141
	v_cvt_pk_f16_f32 v141, v142, v143
	s_waitcnt vmcnt(18)
	v_cvt_pk_f16_f32 v142, v144, v145
	v_cvt_pk_f16_f32 v143, v146, v147
	global_store_dwordx4 v[172:173], v[140:143], off sc1
	s_waitcnt vmcnt(17)
	s_nop 0
	v_cvt_pk_f16_f32 v140, v152, v153
	v_cvt_pk_f16_f32 v141, v154, v155
	v_cvt_pk_f16_f32 v142, v148, v149
	v_cvt_pk_f16_f32 v143, v150, v151
	global_store_dwordx4 v[174:175], v[140:143], off sc1
	s_waitcnt vmcnt(17)
	s_nop 0
	v_cvt_pk_f16_f32 v140, v156, v157
	v_cvt_pk_f16_f32 v141, v158, v159
	s_waitcnt vmcnt(16)
	v_cvt_pk_f16_f32 v142, v160, v161
	v_cvt_pk_f16_f32 v143, v162, v163
	global_store_dwordx4 v[176:177], v[140:143], off sc1
	s_waitcnt vmcnt(16)
	s_nop 0
	v_cvt_pk_f16_f32 v140, v164, v165
	v_cvt_pk_f16_f32 v141, v166, v167
	s_waitcnt vmcnt(15)
	v_cvt_pk_f16_f32 v142, v168, v169
	v_cvt_pk_f16_f32 v143, v170, v171
	global_store_dwordx4 v[178:179], v[140:143], off sc1
	s_cmp_lg_u32 s79, 0
	s_cbranch_scc1 .LBB1_41
	s_mov_b32 s79, 1
	v_mov_b32_e32 v0, v230
	s_branch .LBB1_39
